# GEMM loops: removed the back-to-back s_setprio 0/1 flip pair in the middle of every MFMA segment (36 sites)
# baseline (speedup 1.0000x reference)
.Lwa_186p_0:
	s_waitcnt lgkmcnt(0)
	s_barrier
	s_setprio 1
	s_waitcnt lgkmcnt(0)
	v_mfma_scale_f32_16x16x128_f8f6f4 v[158:161], v[26:33], v[196:203], 0, v194, v194 op_sel_hi:[0,0,0]
	v_mfma_scale_f32_16x16x128_f8f6f4 v[154:157], v[18:25], v[196:203], 0, v194, v194 op_sel_hi:[0,0,0]
	v_mfma_scale_f32_16x16x128_f8f6f4 v[142:145], v[26:33], v[204:211], 0, v194, v194 op_sel_hi:[0,0,0]
	v_mfma_scale_f32_16x16x128_f8f6f4 v[138:141], v[18:25], v[204:211], 0, v194, v194 op_sel_hi:[0,0,0]
	v_mfma_scale_f32_16x16x128_f8f6f4 v[126:129], v[26:33], v[212:219], 0, v194, v194 op_sel_hi:[0,0,0]
	v_mfma_scale_f32_16x16x128_f8f6f4 v[122:125], v[18:25], v[212:219], 0, v194, v194 op_sel_hi:[0,0,0]
	v_mfma_scale_f32_16x16x128_f8f6f4 v[110:113], v[26:33], v[220:227], 0, v194, v194 op_sel_hi:[0,0,0]
	v_mfma_scale_f32_16x16x128_f8f6f4 v[106:109], v[18:25], v[220:227], 0, v194, v194 op_sel_hi:[0,0,0]
	v_mfma_scale_f32_16x16x128_f8f6f4 v[150:153], v[10:17], v[196:203], 0, v194, v194 op_sel_hi:[0,0,0]
	v_mfma_scale_f32_16x16x128_f8f6f4 v[146:149], v[2:9], v[196:203], 0, v194, v194 op_sel_hi:[0,0,0]
	v_mfma_scale_f32_16x16x128_f8f6f4 v[134:137], v[10:17], v[204:211], 0, v194, v194 op_sel_hi:[0,0,0]
	v_mfma_scale_f32_16x16x128_f8f6f4 v[130:133], v[2:9], v[204:211], 0, v194, v194 op_sel_hi:[0,0,0]
	v_mfma_scale_f32_16x16x128_f8f6f4 v[118:121], v[10:17], v[212:219], 0, v194, v194 op_sel_hi:[0,0,0]
	v_mfma_scale_f32_16x16x128_f8f6f4 v[114:117], v[2:9], v[212:219], 0, v194, v194 op_sel_hi:[0,0,0]
	v_mfma_scale_f32_16x16x128_f8f6f4 v[102:105], v[10:17], v[220:227], 0, v194, v194 op_sel_hi:[0,0,0]
	v_mfma_scale_f32_16x16x128_f8f6f4 v[98:101], v[2:9], v[220:227], 0, v194, v194 op_sel_hi:[0,0,0]
	s_cbranch_vccz .Lwb_186p_0
	s_waitcnt vmcnt(8)

.Lwa_186p_1:
	s_waitcnt lgkmcnt(0)
	s_barrier
	s_setprio 1
	s_waitcnt lgkmcnt(0)
	v_mfma_scale_f32_16x16x128_f8f6f4 v[94:97], v[26:33], v[196:203], 0, v194, v194 op_sel_hi:[0,0,0]
	v_mfma_scale_f32_16x16x128_f8f6f4 v[90:93], v[18:25], v[196:203], 0, v194, v194 op_sel_hi:[0,0,0]
	v_mfma_scale_f32_16x16x128_f8f6f4 v[78:81], v[26:33], v[204:211], 0, v194, v194 op_sel_hi:[0,0,0]
	v_mfma_scale_f32_16x16x128_f8f6f4 v[74:77], v[18:25], v[204:211], 0, v194, v194 op_sel_hi:[0,0,0]
	v_mfma_scale_f32_16x16x128_f8f6f4 v[62:65], v[26:33], v[212:219], 0, v194, v194 op_sel_hi:[0,0,0]
	v_mfma_scale_f32_16x16x128_f8f6f4 v[58:61], v[18:25], v[212:219], 0, v194, v194 op_sel_hi:[0,0,0]
	v_mfma_scale_f32_16x16x128_f8f6f4 v[46:49], v[26:33], v[220:227], 0, v194, v194 op_sel_hi:[0,0,0]
	v_mfma_scale_f32_16x16x128_f8f6f4 v[42:45], v[18:25], v[220:227], 0, v194, v194 op_sel_hi:[0,0,0]
	v_mfma_scale_f32_16x16x128_f8f6f4 v[86:89], v[10:17], v[196:203], 0, v194, v194 op_sel_hi:[0,0,0]
	v_mfma_scale_f32_16x16x128_f8f6f4 v[82:85], v[2:9], v[196:203], 0, v194, v194 op_sel_hi:[0,0,0]
	v_mfma_scale_f32_16x16x128_f8f6f4 v[70:73], v[10:17], v[204:211], 0, v194, v194 op_sel_hi:[0,0,0]
	v_mfma_scale_f32_16x16x128_f8f6f4 v[66:69], v[2:9], v[204:211], 0, v194, v194 op_sel_hi:[0,0,0]
	v_mfma_scale_f32_16x16x128_f8f6f4 v[54:57], v[10:17], v[212:219], 0, v194, v194 op_sel_hi:[0,0,0]
	v_mfma_scale_f32_16x16x128_f8f6f4 v[50:53], v[2:9], v[212:219], 0, v194, v194 op_sel_hi:[0,0,0]
	v_mfma_scale_f32_16x16x128_f8f6f4 v[38:41], v[10:17], v[220:227], 0, v194, v194 op_sel_hi:[0,0,0]
	v_mfma_scale_f32_16x16x128_f8f6f4 v[34:37], v[2:9], v[220:227], 0, v194, v194 op_sel_hi:[0,0,0]
	s_cbranch_vccz .Lwb_186p_1
	s_waitcnt vmcnt(8)

.Lwa_186l_0:
	s_waitcnt lgkmcnt(0)
	s_barrier
	s_setprio 1
	s_waitcnt lgkmcnt(0)
	v_mfma_scale_f32_16x16x128_f8f6f4 v[158:161], v[26:33], v[196:203], v[158:161], v194, v194 op_sel_hi:[0,0,0]
	v_mfma_scale_f32_16x16x128_f8f6f4 v[154:157], v[18:25], v[196:203], v[154:157], v194, v194 op_sel_hi:[0,0,0]
	v_mfma_scale_f32_16x16x128_f8f6f4 v[142:145], v[26:33], v[204:211], v[142:145], v194, v194 op_sel_hi:[0,0,0]
	v_mfma_scale_f32_16x16x128_f8f6f4 v[138:141], v[18:25], v[204:211], v[138:141], v194, v194 op_sel_hi:[0,0,0]
	v_mfma_scale_f32_16x16x128_f8f6f4 v[126:129], v[26:33], v[212:219], v[126:129], v194, v194 op_sel_hi:[0,0,0]
	v_mfma_scale_f32_16x16x128_f8f6f4 v[122:125], v[18:25], v[212:219], v[122:125], v194, v194 op_sel_hi:[0,0,0]
	v_mfma_scale_f32_16x16x128_f8f6f4 v[110:113], v[26:33], v[220:227], v[110:113], v194, v194 op_sel_hi:[0,0,0]
	v_mfma_scale_f32_16x16x128_f8f6f4 v[106:109], v[18:25], v[220:227], v[106:109], v194, v194 op_sel_hi:[0,0,0]
	v_mfma_scale_f32_16x16x128_f8f6f4 v[150:153], v[10:17], v[196:203], v[150:153], v194, v194 op_sel_hi:[0,0,0]
	v_mfma_scale_f32_16x16x128_f8f6f4 v[146:149], v[2:9], v[196:203], v[146:149], v194, v194 op_sel_hi:[0,0,0]
	v_mfma_scale_f32_16x16x128_f8f6f4 v[134:137], v[10:17], v[204:211], v[134:137], v194, v194 op_sel_hi:[0,0,0]
	v_mfma_scale_f32_16x16x128_f8f6f4 v[130:133], v[2:9], v[204:211], v[130:133], v194, v194 op_sel_hi:[0,0,0]
	v_mfma_scale_f32_16x16x128_f8f6f4 v[118:121], v[10:17], v[212:219], v[118:121], v194, v194 op_sel_hi:[0,0,0]
	v_mfma_scale_f32_16x16x128_f8f6f4 v[114:117], v[2:9], v[212:219], v[114:117], v194, v194 op_sel_hi:[0,0,0]
	v_mfma_scale_f32_16x16x128_f8f6f4 v[102:105], v[10:17], v[220:227], v[102:105], v194, v194 op_sel_hi:[0,0,0]
	v_mfma_scale_f32_16x16x128_f8f6f4 v[98:101], v[2:9], v[220:227], v[98:101], v194, v194 op_sel_hi:[0,0,0]
	s_cbranch_vccz .Lwb_186l_0
	s_waitcnt vmcnt(8)

.Lwa_186l_1:
	s_waitcnt lgkmcnt(0)
	s_barrier
	s_setprio 1
	s_waitcnt lgkmcnt(0)
	v_mfma_scale_f32_16x16x128_f8f6f4 v[94:97], v[26:33], v[196:203], v[94:97], v194, v194 op_sel_hi:[0,0,0]
	v_mfma_scale_f32_16x16x128_f8f6f4 v[90:93], v[18:25], v[196:203], v[90:93], v194, v194 op_sel_hi:[0,0,0]
	v_mfma_scale_f32_16x16x128_f8f6f4 v[78:81], v[26:33], v[204:211], v[78:81], v194, v194 op_sel_hi:[0,0,0]
	v_mfma_scale_f32_16x16x128_f8f6f4 v[74:77], v[18:25], v[204:211], v[74:77], v194, v194 op_sel_hi:[0,0,0]
	v_mfma_scale_f32_16x16x128_f8f6f4 v[62:65], v[26:33], v[212:219], v[62:65], v194, v194 op_sel_hi:[0,0,0]
	v_mfma_scale_f32_16x16x128_f8f6f4 v[58:61], v[18:25], v[212:219], v[58:61], v194, v194 op_sel_hi:[0,0,0]
	v_mfma_scale_f32_16x16x128_f8f6f4 v[46:49], v[26:33], v[220:227], v[46:49], v194, v194 op_sel_hi:[0,0,0]
	v_mfma_scale_f32_16x16x128_f8f6f4 v[42:45], v[18:25], v[220:227], v[42:45], v194, v194 op_sel_hi:[0,0,0]
	v_mfma_scale_f32_16x16x128_f8f6f4 v[86:89], v[10:17], v[196:203], v[86:89], v194, v194 op_sel_hi:[0,0,0]
	v_mfma_scale_f32_16x16x128_f8f6f4 v[82:85], v[2:9], v[196:203], v[82:85], v194, v194 op_sel_hi:[0,0,0]
	v_mfma_scale_f32_16x16x128_f8f6f4 v[70:73], v[10:17], v[204:211], v[70:73], v194, v194 op_sel_hi:[0,0,0]
	v_mfma_scale_f32_16x16x128_f8f6f4 v[66:69], v[2:9], v[204:211], v[66:69], v194, v194 op_sel_hi:[0,0,0]
	v_mfma_scale_f32_16x16x128_f8f6f4 v[54:57], v[10:17], v[212:219], v[54:57], v194, v194 op_sel_hi:[0,0,0]
	v_mfma_scale_f32_16x16x128_f8f6f4 v[50:53], v[2:9], v[212:219], v[50:53], v194, v194 op_sel_hi:[0,0,0]
	v_mfma_scale_f32_16x16x128_f8f6f4 v[38:41], v[10:17], v[220:227], v[38:41], v194, v194 op_sel_hi:[0,0,0]
	v_mfma_scale_f32_16x16x128_f8f6f4 v[34:37], v[2:9], v[220:227], v[34:37], v194, v194 op_sel_hi:[0,0,0]
	s_cbranch_vccz .Lwb_186l_1
	s_waitcnt vmcnt(8)

.Lwa_186l_2:
	s_waitcnt lgkmcnt(0)
	s_barrier
	s_setprio 1
	s_waitcnt lgkmcnt(0)
	v_mfma_scale_f32_16x16x128_f8f6f4 v[158:161], v[2:9], v[196:203], v[158:161], v194, v194 op_sel_hi:[0,0,0]
	v_mfma_scale_f32_16x16x128_f8f6f4 v[154:157], v[10:17], v[196:203], v[154:157], v194, v194 op_sel_hi:[0,0,0]
	v_mfma_scale_f32_16x16x128_f8f6f4 v[142:145], v[2:9], v[204:211], v[142:145], v194, v194 op_sel_hi:[0,0,0]
	v_mfma_scale_f32_16x16x128_f8f6f4 v[138:141], v[10:17], v[204:211], v[138:141], v194, v194 op_sel_hi:[0,0,0]
	v_mfma_scale_f32_16x16x128_f8f6f4 v[126:129], v[2:9], v[212:219], v[126:129], v194, v194 op_sel_hi:[0,0,0]
	v_mfma_scale_f32_16x16x128_f8f6f4 v[122:125], v[10:17], v[212:219], v[122:125], v194, v194 op_sel_hi:[0,0,0]
	v_mfma_scale_f32_16x16x128_f8f6f4 v[110:113], v[2:9], v[220:227], v[110:113], v194, v194 op_sel_hi:[0,0,0]
	v_mfma_scale_f32_16x16x128_f8f6f4 v[106:109], v[10:17], v[220:227], v[106:109], v194, v194 op_sel_hi:[0,0,0]
	v_mfma_scale_f32_16x16x128_f8f6f4 v[150:153], v[18:25], v[196:203], v[150:153], v194, v194 op_sel_hi:[0,0,0]
	v_mfma_scale_f32_16x16x128_f8f6f4 v[146:149], v[26:33], v[196:203], v[146:149], v194, v194 op_sel_hi:[0,0,0]
	v_mfma_scale_f32_16x16x128_f8f6f4 v[134:137], v[18:25], v[204:211], v[134:137], v194, v194 op_sel_hi:[0,0,0]
	v_mfma_scale_f32_16x16x128_f8f6f4 v[130:133], v[26:33], v[204:211], v[130:133], v194, v194 op_sel_hi:[0,0,0]
	v_mfma_scale_f32_16x16x128_f8f6f4 v[118:121], v[18:25], v[212:219], v[118:121], v194, v194 op_sel_hi:[0,0,0]
	v_mfma_scale_f32_16x16x128_f8f6f4 v[114:117], v[26:33], v[212:219], v[114:117], v194, v194 op_sel_hi:[0,0,0]
	v_mfma_scale_f32_16x16x128_f8f6f4 v[102:105], v[18:25], v[220:227], v[102:105], v194, v194 op_sel_hi:[0,0,0]
	v_mfma_scale_f32_16x16x128_f8f6f4 v[98:101], v[26:33], v[220:227], v[98:101], v194, v194 op_sel_hi:[0,0,0]
	s_cbranch_vccz .Lwb_186l_2
	s_waitcnt vmcnt(8)

.Lwa_186l_3:
	s_waitcnt lgkmcnt(0)
	s_barrier
	s_setprio 1
	s_waitcnt lgkmcnt(0)
	v_mfma_scale_f32_16x16x128_f8f6f4 v[94:97], v[2:9], v[196:203], v[94:97], v194, v194 op_sel_hi:[0,0,0]
	v_mfma_scale_f32_16x16x128_f8f6f4 v[90:93], v[10:17], v[196:203], v[90:93], v194, v194 op_sel_hi:[0,0,0]
	v_mfma_scale_f32_16x16x128_f8f6f4 v[78:81], v[2:9], v[204:211], v[78:81], v194, v194 op_sel_hi:[0,0,0]
	v_mfma_scale_f32_16x16x128_f8f6f4 v[74:77], v[10:17], v[204:211], v[74:77], v194, v194 op_sel_hi:[0,0,0]
	v_mfma_scale_f32_16x16x128_f8f6f4 v[62:65], v[2:9], v[212:219], v[62:65], v194, v194 op_sel_hi:[0,0,0]
	v_mfma_scale_f32_16x16x128_f8f6f4 v[58:61], v[10:17], v[212:219], v[58:61], v194, v194 op_sel_hi:[0,0,0]
	v_mfma_scale_f32_16x16x128_f8f6f4 v[46:49], v[2:9], v[220:227], v[46:49], v194, v194 op_sel_hi:[0,0,0]
	v_mfma_scale_f32_16x16x128_f8f6f4 v[42:45], v[10:17], v[220:227], v[42:45], v194, v194 op_sel_hi:[0,0,0]
	v_mfma_scale_f32_16x16x128_f8f6f4 v[86:89], v[18:25], v[196:203], v[86:89], v194, v194 op_sel_hi:[0,0,0]
	v_mfma_scale_f32_16x16x128_f8f6f4 v[82:85], v[26:33], v[196:203], v[82:85], v194, v194 op_sel_hi:[0,0,0]
	v_mfma_scale_f32_16x16x128_f8f6f4 v[70:73], v[18:25], v[204:211], v[70:73], v194, v194 op_sel_hi:[0,0,0]
	v_mfma_scale_f32_16x16x128_f8f6f4 v[66:69], v[26:33], v[204:211], v[66:69], v194, v194 op_sel_hi:[0,0,0]
	v_mfma_scale_f32_16x16x128_f8f6f4 v[54:57], v[18:25], v[212:219], v[54:57], v194, v194 op_sel_hi:[0,0,0]
	v_mfma_scale_f32_16x16x128_f8f6f4 v[50:53], v[26:33], v[212:219], v[50:53], v194, v194 op_sel_hi:[0,0,0]
	v_mfma_scale_f32_16x16x128_f8f6f4 v[38:41], v[18:25], v[220:227], v[38:41], v194, v194 op_sel_hi:[0,0,0]
	v_mfma_scale_f32_16x16x128_f8f6f4 v[34:37], v[26:33], v[220:227], v[34:37], v194, v194 op_sel_hi:[0,0,0]
	s_cbranch_vccz .Lwb_186l_3
	s_waitcnt vmcnt(8)

.Lwa_1129p_0:
	s_waitcnt lgkmcnt(0)
	s_barrier
	s_setprio 1
	s_waitcnt lgkmcnt(0)
	v_mfma_f32_16x16x32_bf16 v[126:129], v[146:149], v[192:195], 0
	v_mfma_f32_16x16x32_bf16 v[122:125], v[168:171], v[192:195], 0
	v_mfma_f32_16x16x32_bf16 v[110:113], v[146:149], v[200:203], 0
	v_mfma_f32_16x16x32_bf16 v[106:109], v[168:171], v[200:203], 0
	v_mfma_f32_16x16x32_bf16 v[94:97], v[146:149], v[208:211], 0
	v_mfma_f32_16x16x32_bf16 v[90:93], v[168:171], v[208:211], 0
	v_mfma_f32_16x16x32_bf16 v[78:81], v[146:149], v[216:219], 0
	v_mfma_f32_16x16x32_bf16 v[74:77], v[168:171], v[216:219], 0
	v_mfma_f32_16x16x32_bf16 v[126:129], v[150:153], v[196:199], v[126:129]
	v_mfma_f32_16x16x32_bf16 v[122:125], v[172:175], v[196:199], v[122:125]
	v_mfma_f32_16x16x32_bf16 v[110:113], v[150:153], v[204:207], v[110:113]
	v_mfma_f32_16x16x32_bf16 v[106:109], v[172:175], v[204:207], v[106:109]
	v_mfma_f32_16x16x32_bf16 v[94:97], v[150:153], v[212:215], v[94:97]
	v_mfma_f32_16x16x32_bf16 v[90:93], v[172:175], v[212:215], v[90:93]
	v_mfma_f32_16x16x32_bf16 v[78:81], v[150:153], v[220:223], v[78:81]
	v_mfma_f32_16x16x32_bf16 v[74:77], v[172:175], v[220:223], v[74:77]
	v_mfma_f32_16x16x32_bf16 v[118:121], v[176:179], v[192:195], 0
	v_mfma_f32_16x16x32_bf16 v[114:117], v[184:187], v[192:195], 0
	v_mfma_f32_16x16x32_bf16 v[102:105], v[176:179], v[200:203], 0
	v_mfma_f32_16x16x32_bf16 v[98:101], v[184:187], v[200:203], 0
	v_mfma_f32_16x16x32_bf16 v[86:89], v[176:179], v[208:211], 0
	v_mfma_f32_16x16x32_bf16 v[82:85], v[184:187], v[208:211], 0
	v_mfma_f32_16x16x32_bf16 v[70:73], v[176:179], v[216:219], 0
	v_mfma_f32_16x16x32_bf16 v[66:69], v[184:187], v[216:219], 0
	v_mfma_f32_16x16x32_bf16 v[118:121], v[180:183], v[196:199], v[118:121]
	v_mfma_f32_16x16x32_bf16 v[114:117], v[188:191], v[196:199], v[114:117]
	v_mfma_f32_16x16x32_bf16 v[102:105], v[180:183], v[204:207], v[102:105]
	v_mfma_f32_16x16x32_bf16 v[98:101], v[188:191], v[204:207], v[98:101]
	v_mfma_f32_16x16x32_bf16 v[86:89], v[180:183], v[212:215], v[86:89]
	v_mfma_f32_16x16x32_bf16 v[82:85], v[188:191], v[212:215], v[82:85]
	v_mfma_f32_16x16x32_bf16 v[70:73], v[180:183], v[220:223], v[70:73]
	v_mfma_f32_16x16x32_bf16 v[66:69], v[188:191], v[220:223], v[66:69]
	s_cbranch_vccz .Lwb_1129p_0
	s_waitcnt vmcnt(8)

.Lwa_1129p_1:
	s_waitcnt lgkmcnt(0)
	s_barrier
	s_setprio 1
	s_waitcnt lgkmcnt(0)
	v_mfma_f32_16x16x32_bf16 v[62:65], v[146:149], v[192:195], 0
	v_mfma_f32_16x16x32_bf16 v[58:61], v[168:171], v[192:195], 0
	v_mfma_f32_16x16x32_bf16 v[46:49], v[146:149], v[200:203], 0
	v_mfma_f32_16x16x32_bf16 v[42:45], v[168:171], v[200:203], 0
	v_mfma_f32_16x16x32_bf16 v[30:33], v[146:149], v[208:211], 0
	v_mfma_f32_16x16x32_bf16 v[26:29], v[168:171], v[208:211], 0
	v_mfma_f32_16x16x32_bf16 v[14:17], v[146:149], v[216:219], 0
	v_mfma_f32_16x16x32_bf16 v[10:13], v[168:171], v[216:219], 0
	v_mfma_f32_16x16x32_bf16 v[62:65], v[150:153], v[196:199], v[62:65]
	v_mfma_f32_16x16x32_bf16 v[58:61], v[172:175], v[196:199], v[58:61]
	v_mfma_f32_16x16x32_bf16 v[46:49], v[150:153], v[204:207], v[46:49]
	v_mfma_f32_16x16x32_bf16 v[42:45], v[172:175], v[204:207], v[42:45]
	v_mfma_f32_16x16x32_bf16 v[30:33], v[150:153], v[212:215], v[30:33]
	v_mfma_f32_16x16x32_bf16 v[26:29], v[172:175], v[212:215], v[26:29]
	v_mfma_f32_16x16x32_bf16 v[14:17], v[150:153], v[220:223], v[14:17]
	v_mfma_f32_16x16x32_bf16 v[10:13], v[172:175], v[220:223], v[10:13]
	v_mfma_f32_16x16x32_bf16 v[54:57], v[176:179], v[192:195], 0
	v_mfma_f32_16x16x32_bf16 v[50:53], v[184:187], v[192:195], 0
	v_mfma_f32_16x16x32_bf16 v[38:41], v[176:179], v[200:203], 0
	v_mfma_f32_16x16x32_bf16 v[34:37], v[184:187], v[200:203], 0
	v_mfma_f32_16x16x32_bf16 v[22:25], v[176:179], v[208:211], 0
	v_mfma_f32_16x16x32_bf16 v[18:21], v[184:187], v[208:211], 0
	v_mfma_f32_16x16x32_bf16 v[6:9], v[176:179], v[216:219], 0
	v_mfma_f32_16x16x32_bf16 v[2:5], v[184:187], v[216:219], 0
	v_mfma_f32_16x16x32_bf16 v[54:57], v[180:183], v[196:199], v[54:57]
	v_mfma_f32_16x16x32_bf16 v[50:53], v[188:191], v[196:199], v[50:53]
	v_mfma_f32_16x16x32_bf16 v[38:41], v[180:183], v[204:207], v[38:41]
	v_mfma_f32_16x16x32_bf16 v[34:37], v[188:191], v[204:207], v[34:37]
	v_mfma_f32_16x16x32_bf16 v[22:25], v[180:183], v[212:215], v[22:25]
	v_mfma_f32_16x16x32_bf16 v[18:21], v[188:191], v[212:215], v[18:21]
	v_mfma_f32_16x16x32_bf16 v[6:9], v[180:183], v[220:223], v[6:9]
	v_mfma_f32_16x16x32_bf16 v[2:5], v[188:191], v[220:223], v[2:5]
	s_cbranch_vccz .Lwb_1129p_1
	s_waitcnt vmcnt(8)

.Lwa_1129l_0:
	s_waitcnt lgkmcnt(0)
	s_barrier
	s_setprio 1
	s_waitcnt lgkmcnt(0)
	v_mfma_f32_16x16x32_bf16 v[126:129], v[146:149], v[192:195], v[126:129]
	v_mfma_f32_16x16x32_bf16 v[122:125], v[168:171], v[192:195], v[122:125]
	v_mfma_f32_16x16x32_bf16 v[110:113], v[146:149], v[200:203], v[110:113]
	v_mfma_f32_16x16x32_bf16 v[106:109], v[168:171], v[200:203], v[106:109]
	v_mfma_f32_16x16x32_bf16 v[94:97], v[146:149], v[208:211], v[94:97]
	v_mfma_f32_16x16x32_bf16 v[90:93], v[168:171], v[208:211], v[90:93]
	v_mfma_f32_16x16x32_bf16 v[78:81], v[146:149], v[216:219], v[78:81]
	v_mfma_f32_16x16x32_bf16 v[74:77], v[168:171], v[216:219], v[74:77]
	v_mfma_f32_16x16x32_bf16 v[126:129], v[150:153], v[196:199], v[126:129]
	v_mfma_f32_16x16x32_bf16 v[122:125], v[172:175], v[196:199], v[122:125]
	v_mfma_f32_16x16x32_bf16 v[110:113], v[150:153], v[204:207], v[110:113]
	v_mfma_f32_16x16x32_bf16 v[106:109], v[172:175], v[204:207], v[106:109]
	v_mfma_f32_16x16x32_bf16 v[94:97], v[150:153], v[212:215], v[94:97]
	v_mfma_f32_16x16x32_bf16 v[90:93], v[172:175], v[212:215], v[90:93]
	v_mfma_f32_16x16x32_bf16 v[78:81], v[150:153], v[220:223], v[78:81]
	v_mfma_f32_16x16x32_bf16 v[74:77], v[172:175], v[220:223], v[74:77]
	v_mfma_f32_16x16x32_bf16 v[118:121], v[176:179], v[192:195], v[118:121]
	v_mfma_f32_16x16x32_bf16 v[114:117], v[184:187], v[192:195], v[114:117]
	v_mfma_f32_16x16x32_bf16 v[102:105], v[176:179], v[200:203], v[102:105]
	v_mfma_f32_16x16x32_bf16 v[98:101], v[184:187], v[200:203], v[98:101]
	v_mfma_f32_16x16x32_bf16 v[86:89], v[176:179], v[208:211], v[86:89]
	v_mfma_f32_16x16x32_bf16 v[82:85], v[184:187], v[208:211], v[82:85]
	v_mfma_f32_16x16x32_bf16 v[70:73], v[176:179], v[216:219], v[70:73]
	v_mfma_f32_16x16x32_bf16 v[66:69], v[184:187], v[216:219], v[66:69]
	v_mfma_f32_16x16x32_bf16 v[118:121], v[180:183], v[196:199], v[118:121]
	v_mfma_f32_16x16x32_bf16 v[114:117], v[188:191], v[196:199], v[114:117]
	v_mfma_f32_16x16x32_bf16 v[102:105], v[180:183], v[204:207], v[102:105]
	v_mfma_f32_16x16x32_bf16 v[98:101], v[188:191], v[204:207], v[98:101]
	v_mfma_f32_16x16x32_bf16 v[86:89], v[180:183], v[212:215], v[86:89]
	v_mfma_f32_16x16x32_bf16 v[82:85], v[188:191], v[212:215], v[82:85]
	v_mfma_f32_16x16x32_bf16 v[70:73], v[180:183], v[220:223], v[70:73]
	v_mfma_f32_16x16x32_bf16 v[66:69], v[188:191], v[220:223], v[66:69]
	s_cbranch_vccz .Lwb_1129l_0
	s_waitcnt vmcnt(8)

.Lwa_1129l_1:
	s_waitcnt lgkmcnt(0)
	s_barrier
	s_setprio 1
	s_waitcnt lgkmcnt(0)
	v_mfma_f32_16x16x32_bf16 v[62:65], v[146:149], v[192:195], v[62:65]
	v_mfma_f32_16x16x32_bf16 v[58:61], v[168:171], v[192:195], v[58:61]
	v_mfma_f32_16x16x32_bf16 v[46:49], v[146:149], v[200:203], v[46:49]
	v_mfma_f32_16x16x32_bf16 v[42:45], v[168:171], v[200:203], v[42:45]
	v_mfma_f32_16x16x32_bf16 v[30:33], v[146:149], v[208:211], v[30:33]
	v_mfma_f32_16x16x32_bf16 v[26:29], v[168:171], v[208:211], v[26:29]
	v_mfma_f32_16x16x32_bf16 v[14:17], v[146:149], v[216:219], v[14:17]
	v_mfma_f32_16x16x32_bf16 v[10:13], v[168:171], v[216:219], v[10:13]
	v_mfma_f32_16x16x32_bf16 v[62:65], v[150:153], v[196:199], v[62:65]
	v_mfma_f32_16x16x32_bf16 v[58:61], v[172:175], v[196:199], v[58:61]
	v_mfma_f32_16x16x32_bf16 v[46:49], v[150:153], v[204:207], v[46:49]
	v_mfma_f32_16x16x32_bf16 v[42:45], v[172:175], v[204:207], v[42:45]
	v_mfma_f32_16x16x32_bf16 v[30:33], v[150:153], v[212:215], v[30:33]
	v_mfma_f32_16x16x32_bf16 v[26:29], v[172:175], v[212:215], v[26:29]
	v_mfma_f32_16x16x32_bf16 v[14:17], v[150:153], v[220:223], v[14:17]
	v_mfma_f32_16x16x32_bf16 v[10:13], v[172:175], v[220:223], v[10:13]
	v_mfma_f32_16x16x32_bf16 v[54:57], v[176:179], v[192:195], v[54:57]
	v_mfma_f32_16x16x32_bf16 v[50:53], v[184:187], v[192:195], v[50:53]
	v_mfma_f32_16x16x32_bf16 v[38:41], v[176:179], v[200:203], v[38:41]
	v_mfma_f32_16x16x32_bf16 v[34:37], v[184:187], v[200:203], v[34:37]
	v_mfma_f32_16x16x32_bf16 v[22:25], v[176:179], v[208:211], v[22:25]
	v_mfma_f32_16x16x32_bf16 v[18:21], v[184:187], v[208:211], v[18:21]
	v_mfma_f32_16x16x32_bf16 v[6:9], v[176:179], v[216:219], v[6:9]
	v_mfma_f32_16x16x32_bf16 v[2:5], v[184:187], v[216:219], v[2:5]
	v_mfma_f32_16x16x32_bf16 v[54:57], v[180:183], v[196:199], v[54:57]
	v_mfma_f32_16x16x32_bf16 v[50:53], v[188:191], v[196:199], v[50:53]
	v_mfma_f32_16x16x32_bf16 v[38:41], v[180:183], v[204:207], v[38:41]
	v_mfma_f32_16x16x32_bf16 v[34:37], v[188:191], v[204:207], v[34:37]
	v_mfma_f32_16x16x32_bf16 v[22:25], v[180:183], v[212:215], v[22:25]
	v_mfma_f32_16x16x32_bf16 v[18:21], v[188:191], v[212:215], v[18:21]
	v_mfma_f32_16x16x32_bf16 v[6:9], v[180:183], v[220:223], v[6:9]
	v_mfma_f32_16x16x32_bf16 v[2:5], v[188:191], v[220:223], v[2:5]
	s_cbranch_vccz .Lwb_1129l_1
	s_waitcnt vmcnt(8)

.Lwa_1153p_0:
	s_waitcnt lgkmcnt(0)
	s_barrier
	s_setprio 1
	s_waitcnt lgkmcnt(0)
	v_mfma_f32_16x16x32_bf16 v[126:129], v[146:149], v[184:187], 0
	v_mfma_f32_16x16x32_bf16 v[122:125], v[160:163], v[184:187], 0
	v_mfma_f32_16x16x32_bf16 v[110:113], v[146:149], v[192:195], 0
	v_mfma_f32_16x16x32_bf16 v[106:109], v[160:163], v[192:195], 0
	v_mfma_f32_16x16x32_bf16 v[94:97], v[146:149], v[200:203], 0
	v_mfma_f32_16x16x32_bf16 v[90:93], v[160:163], v[200:203], 0
	v_mfma_f32_16x16x32_bf16 v[78:81], v[146:149], v[208:211], 0
	v_mfma_f32_16x16x32_bf16 v[74:77], v[160:163], v[208:211], 0
	v_mfma_f32_16x16x32_bf16 v[126:129], v[150:153], v[188:191], v[126:129]
	v_mfma_f32_16x16x32_bf16 v[122:125], v[164:167], v[188:191], v[122:125]
	v_mfma_f32_16x16x32_bf16 v[110:113], v[150:153], v[196:199], v[110:113]
	v_mfma_f32_16x16x32_bf16 v[106:109], v[164:167], v[196:199], v[106:109]
	v_mfma_f32_16x16x32_bf16 v[94:97], v[150:153], v[204:207], v[94:97]
	v_mfma_f32_16x16x32_bf16 v[90:93], v[164:167], v[204:207], v[90:93]
	v_mfma_f32_16x16x32_bf16 v[78:81], v[150:153], v[212:215], v[78:81]
	v_mfma_f32_16x16x32_bf16 v[74:77], v[164:167], v[212:215], v[74:77]
	v_mfma_f32_16x16x32_bf16 v[118:121], v[168:171], v[184:187], 0
	v_mfma_f32_16x16x32_bf16 v[114:117], v[176:179], v[184:187], 0
	v_mfma_f32_16x16x32_bf16 v[102:105], v[168:171], v[192:195], 0
	v_mfma_f32_16x16x32_bf16 v[98:101], v[176:179], v[192:195], 0
	v_mfma_f32_16x16x32_bf16 v[86:89], v[168:171], v[200:203], 0
	v_mfma_f32_16x16x32_bf16 v[82:85], v[176:179], v[200:203], 0
	v_mfma_f32_16x16x32_bf16 v[70:73], v[168:171], v[208:211], 0
	v_mfma_f32_16x16x32_bf16 v[66:69], v[176:179], v[208:211], 0
	v_mfma_f32_16x16x32_bf16 v[118:121], v[172:175], v[188:191], v[118:121]
	v_mfma_f32_16x16x32_bf16 v[114:117], v[180:183], v[188:191], v[114:117]
	v_mfma_f32_16x16x32_bf16 v[102:105], v[172:175], v[196:199], v[102:105]
	v_mfma_f32_16x16x32_bf16 v[98:101], v[180:183], v[196:199], v[98:101]
	v_mfma_f32_16x16x32_bf16 v[86:89], v[172:175], v[204:207], v[86:89]
	v_mfma_f32_16x16x32_bf16 v[82:85], v[180:183], v[204:207], v[82:85]
	v_mfma_f32_16x16x32_bf16 v[70:73], v[172:175], v[212:215], v[70:73]
	v_mfma_f32_16x16x32_bf16 v[66:69], v[180:183], v[212:215], v[66:69]
	s_cbranch_vccz .Lwb_1153p_0
	s_waitcnt vmcnt(8)

.Lwa_1153p_1:
	s_waitcnt lgkmcnt(0)
	s_barrier
	s_setprio 1
	s_waitcnt lgkmcnt(0)
	v_mfma_f32_16x16x32_bf16 v[62:65], v[146:149], v[184:187], 0
	v_mfma_f32_16x16x32_bf16 v[58:61], v[160:163], v[184:187], 0
	v_mfma_f32_16x16x32_bf16 v[46:49], v[146:149], v[192:195], 0
	v_mfma_f32_16x16x32_bf16 v[42:45], v[160:163], v[192:195], 0
	v_mfma_f32_16x16x32_bf16 v[30:33], v[146:149], v[200:203], 0
	v_mfma_f32_16x16x32_bf16 v[26:29], v[160:163], v[200:203], 0
	v_mfma_f32_16x16x32_bf16 v[14:17], v[146:149], v[208:211], 0
	v_mfma_f32_16x16x32_bf16 v[10:13], v[160:163], v[208:211], 0
	v_mfma_f32_16x16x32_bf16 v[62:65], v[150:153], v[188:191], v[62:65]
	v_mfma_f32_16x16x32_bf16 v[58:61], v[164:167], v[188:191], v[58:61]
	v_mfma_f32_16x16x32_bf16 v[46:49], v[150:153], v[196:199], v[46:49]
	v_mfma_f32_16x16x32_bf16 v[42:45], v[164:167], v[196:199], v[42:45]
	v_mfma_f32_16x16x32_bf16 v[30:33], v[150:153], v[204:207], v[30:33]
	v_mfma_f32_16x16x32_bf16 v[26:29], v[164:167], v[204:207], v[26:29]
	v_mfma_f32_16x16x32_bf16 v[14:17], v[150:153], v[212:215], v[14:17]
	v_mfma_f32_16x16x32_bf16 v[10:13], v[164:167], v[212:215], v[10:13]
	v_mfma_f32_16x16x32_bf16 v[54:57], v[168:171], v[184:187], 0
	v_mfma_f32_16x16x32_bf16 v[50:53], v[176:179], v[184:187], 0
	v_mfma_f32_16x16x32_bf16 v[38:41], v[168:171], v[192:195], 0
	v_mfma_f32_16x16x32_bf16 v[34:37], v[176:179], v[192:195], 0
	v_mfma_f32_16x16x32_bf16 v[22:25], v[168:171], v[200:203], 0
	v_mfma_f32_16x16x32_bf16 v[18:21], v[176:179], v[200:203], 0
	v_mfma_f32_16x16x32_bf16 v[6:9], v[168:171], v[208:211], 0
	v_mfma_f32_16x16x32_bf16 v[2:5], v[176:179], v[208:211], 0
	v_mfma_f32_16x16x32_bf16 v[54:57], v[172:175], v[188:191], v[54:57]
	v_mfma_f32_16x16x32_bf16 v[50:53], v[180:183], v[188:191], v[50:53]
	v_mfma_f32_16x16x32_bf16 v[38:41], v[172:175], v[196:199], v[38:41]
	v_mfma_f32_16x16x32_bf16 v[34:37], v[180:183], v[196:199], v[34:37]
	v_mfma_f32_16x16x32_bf16 v[22:25], v[172:175], v[204:207], v[22:25]
	v_mfma_f32_16x16x32_bf16 v[18:21], v[180:183], v[204:207], v[18:21]
	v_mfma_f32_16x16x32_bf16 v[6:9], v[172:175], v[212:215], v[6:9]
	v_mfma_f32_16x16x32_bf16 v[2:5], v[180:183], v[212:215], v[2:5]
	s_cbranch_vccz .Lwb_1153p_1
	s_waitcnt vmcnt(8)

.Lwa_1153l_0:
	s_waitcnt lgkmcnt(0)
	s_barrier
	s_setprio 1
	s_waitcnt lgkmcnt(0)
	v_mfma_f32_16x16x32_bf16 v[126:129], v[146:149], v[184:187], v[126:129]
	v_mfma_f32_16x16x32_bf16 v[122:125], v[160:163], v[184:187], v[122:125]
	v_mfma_f32_16x16x32_bf16 v[110:113], v[146:149], v[192:195], v[110:113]
	v_mfma_f32_16x16x32_bf16 v[106:109], v[160:163], v[192:195], v[106:109]
	v_mfma_f32_16x16x32_bf16 v[94:97], v[146:149], v[200:203], v[94:97]
	v_mfma_f32_16x16x32_bf16 v[90:93], v[160:163], v[200:203], v[90:93]
	v_mfma_f32_16x16x32_bf16 v[78:81], v[146:149], v[208:211], v[78:81]
	v_mfma_f32_16x16x32_bf16 v[74:77], v[160:163], v[208:211], v[74:77]
	v_mfma_f32_16x16x32_bf16 v[126:129], v[150:153], v[188:191], v[126:129]
	v_mfma_f32_16x16x32_bf16 v[122:125], v[164:167], v[188:191], v[122:125]
	v_mfma_f32_16x16x32_bf16 v[110:113], v[150:153], v[196:199], v[110:113]
	v_mfma_f32_16x16x32_bf16 v[106:109], v[164:167], v[196:199], v[106:109]
	v_mfma_f32_16x16x32_bf16 v[94:97], v[150:153], v[204:207], v[94:97]
	v_mfma_f32_16x16x32_bf16 v[90:93], v[164:167], v[204:207], v[90:93]
	v_mfma_f32_16x16x32_bf16 v[78:81], v[150:153], v[212:215], v[78:81]
	v_mfma_f32_16x16x32_bf16 v[74:77], v[164:167], v[212:215], v[74:77]
	v_mfma_f32_16x16x32_bf16 v[118:121], v[168:171], v[184:187], v[118:121]
	v_mfma_f32_16x16x32_bf16 v[114:117], v[176:179], v[184:187], v[114:117]
	v_mfma_f32_16x16x32_bf16 v[102:105], v[168:171], v[192:195], v[102:105]
	v_mfma_f32_16x16x32_bf16 v[98:101], v[176:179], v[192:195], v[98:101]
	v_mfma_f32_16x16x32_bf16 v[86:89], v[168:171], v[200:203], v[86:89]
	v_mfma_f32_16x16x32_bf16 v[82:85], v[176:179], v[200:203], v[82:85]
	v_mfma_f32_16x16x32_bf16 v[70:73], v[168:171], v[208:211], v[70:73]
	v_mfma_f32_16x16x32_bf16 v[66:69], v[176:179], v[208:211], v[66:69]
	v_mfma_f32_16x16x32_bf16 v[118:121], v[172:175], v[188:191], v[118:121]
	v_mfma_f32_16x16x32_bf16 v[114:117], v[180:183], v[188:191], v[114:117]
	v_mfma_f32_16x16x32_bf16 v[102:105], v[172:175], v[196:199], v[102:105]
	v_mfma_f32_16x16x32_bf16 v[98:101], v[180:183], v[196:199], v[98:101]
	v_mfma_f32_16x16x32_bf16 v[86:89], v[172:175], v[204:207], v[86:89]
	v_mfma_f32_16x16x32_bf16 v[82:85], v[180:183], v[204:207], v[82:85]
	v_mfma_f32_16x16x32_bf16 v[70:73], v[172:175], v[212:215], v[70:73]
	v_mfma_f32_16x16x32_bf16 v[66:69], v[180:183], v[212:215], v[66:69]
	s_cbranch_vccz .Lwb_1153l_0
	s_waitcnt vmcnt(8)

.Lwa_1153l_1:
	s_waitcnt lgkmcnt(0)
	s_barrier
	s_setprio 1
	s_waitcnt lgkmcnt(0)
	v_mfma_f32_16x16x32_bf16 v[62:65], v[146:149], v[184:187], v[62:65]
	v_mfma_f32_16x16x32_bf16 v[58:61], v[160:163], v[184:187], v[58:61]
	v_mfma_f32_16x16x32_bf16 v[46:49], v[146:149], v[192:195], v[46:49]
	v_mfma_f32_16x16x32_bf16 v[42:45], v[160:163], v[192:195], v[42:45]
	v_mfma_f32_16x16x32_bf16 v[30:33], v[146:149], v[200:203], v[30:33]
	v_mfma_f32_16x16x32_bf16 v[26:29], v[160:163], v[200:203], v[26:29]
	v_mfma_f32_16x16x32_bf16 v[14:17], v[146:149], v[208:211], v[14:17]
	v_mfma_f32_16x16x32_bf16 v[10:13], v[160:163], v[208:211], v[10:13]
	v_mfma_f32_16x16x32_bf16 v[62:65], v[150:153], v[188:191], v[62:65]
	v_mfma_f32_16x16x32_bf16 v[58:61], v[164:167], v[188:191], v[58:61]
	v_mfma_f32_16x16x32_bf16 v[46:49], v[150:153], v[196:199], v[46:49]
	v_mfma_f32_16x16x32_bf16 v[42:45], v[164:167], v[196:199], v[42:45]
	v_mfma_f32_16x16x32_bf16 v[30:33], v[150:153], v[204:207], v[30:33]
	v_mfma_f32_16x16x32_bf16 v[26:29], v[164:167], v[204:207], v[26:29]
	v_mfma_f32_16x16x32_bf16 v[14:17], v[150:153], v[212:215], v[14:17]
	v_mfma_f32_16x16x32_bf16 v[10:13], v[164:167], v[212:215], v[10:13]
	v_mfma_f32_16x16x32_bf16 v[54:57], v[168:171], v[184:187], v[54:57]
	v_mfma_f32_16x16x32_bf16 v[50:53], v[176:179], v[184:187], v[50:53]
	v_mfma_f32_16x16x32_bf16 v[38:41], v[168:171], v[192:195], v[38:41]
	v_mfma_f32_16x16x32_bf16 v[34:37], v[176:179], v[192:195], v[34:37]
	v_mfma_f32_16x16x32_bf16 v[22:25], v[168:171], v[200:203], v[22:25]
	v_mfma_f32_16x16x32_bf16 v[18:21], v[176:179], v[200:203], v[18:21]
	v_mfma_f32_16x16x32_bf16 v[6:9], v[168:171], v[208:211], v[6:9]
	v_mfma_f32_16x16x32_bf16 v[2:5], v[176:179], v[208:211], v[2:5]
	v_mfma_f32_16x16x32_bf16 v[54:57], v[172:175], v[188:191], v[54:57]
	v_mfma_f32_16x16x32_bf16 v[50:53], v[180:183], v[188:191], v[50:53]
	v_mfma_f32_16x16x32_bf16 v[38:41], v[172:175], v[196:199], v[38:41]
	v_mfma_f32_16x16x32_bf16 v[34:37], v[180:183], v[196:199], v[34:37]
	v_mfma_f32_16x16x32_bf16 v[22:25], v[172:175], v[204:207], v[22:25]
	v_mfma_f32_16x16x32_bf16 v[18:21], v[180:183], v[204:207], v[18:21]
	v_mfma_f32_16x16x32_bf16 v[6:9], v[172:175], v[212:215], v[6:9]
	v_mfma_f32_16x16x32_bf16 v[2:5], v[180:183], v[212:215], v[2:5]
	s_cbranch_vccz .Lwb_1153l_1
	s_waitcnt vmcnt(8)

.Lwa_1228p_0:
	s_waitcnt lgkmcnt(0)
	s_barrier
	s_setprio 1
	s_waitcnt lgkmcnt(0)
	v_mfma_f32_16x16x32_bf16 v[126:129], v[146:149], v[186:189], 0
	v_mfma_f32_16x16x32_bf16 v[122:125], v[162:165], v[186:189], 0
	v_mfma_f32_16x16x32_bf16 v[110:113], v[146:149], v[194:197], 0
	v_mfma_f32_16x16x32_bf16 v[106:109], v[162:165], v[194:197], 0
	v_mfma_f32_16x16x32_bf16 v[94:97], v[146:149], v[202:205], 0
	v_mfma_f32_16x16x32_bf16 v[90:93], v[162:165], v[202:205], 0
	v_mfma_f32_16x16x32_bf16 v[78:81], v[146:149], v[210:213], 0
	v_mfma_f32_16x16x32_bf16 v[74:77], v[162:165], v[210:213], 0
	v_mfma_f32_16x16x32_bf16 v[126:129], v[158:161], v[190:193], v[126:129]
	v_mfma_f32_16x16x32_bf16 v[122:125], v[166:169], v[190:193], v[122:125]
	v_mfma_f32_16x16x32_bf16 v[110:113], v[158:161], v[198:201], v[110:113]
	v_mfma_f32_16x16x32_bf16 v[106:109], v[166:169], v[198:201], v[106:109]
	v_mfma_f32_16x16x32_bf16 v[94:97], v[158:161], v[206:209], v[94:97]
	v_mfma_f32_16x16x32_bf16 v[90:93], v[166:169], v[206:209], v[90:93]
	v_mfma_f32_16x16x32_bf16 v[78:81], v[158:161], v[214:217], v[78:81]
	v_mfma_f32_16x16x32_bf16 v[74:77], v[166:169], v[214:217], v[74:77]
	v_mfma_f32_16x16x32_bf16 v[118:121], v[170:173], v[186:189], 0
	v_mfma_f32_16x16x32_bf16 v[114:117], v[178:181], v[186:189], 0
	v_mfma_f32_16x16x32_bf16 v[102:105], v[170:173], v[194:197], 0
	v_mfma_f32_16x16x32_bf16 v[98:101], v[178:181], v[194:197], 0
	v_mfma_f32_16x16x32_bf16 v[86:89], v[170:173], v[202:205], 0
	v_mfma_f32_16x16x32_bf16 v[82:85], v[178:181], v[202:205], 0
	v_mfma_f32_16x16x32_bf16 v[70:73], v[170:173], v[210:213], 0
	v_mfma_f32_16x16x32_bf16 v[66:69], v[178:181], v[210:213], 0
	v_mfma_f32_16x16x32_bf16 v[118:121], v[174:177], v[190:193], v[118:121]
	v_mfma_f32_16x16x32_bf16 v[114:117], v[182:185], v[190:193], v[114:117]
	v_mfma_f32_16x16x32_bf16 v[102:105], v[174:177], v[198:201], v[102:105]
	v_mfma_f32_16x16x32_bf16 v[98:101], v[182:185], v[198:201], v[98:101]
	v_mfma_f32_16x16x32_bf16 v[86:89], v[174:177], v[206:209], v[86:89]
	v_mfma_f32_16x16x32_bf16 v[82:85], v[182:185], v[206:209], v[82:85]
	v_mfma_f32_16x16x32_bf16 v[70:73], v[174:177], v[214:217], v[70:73]
	v_mfma_f32_16x16x32_bf16 v[66:69], v[182:185], v[214:217], v[66:69]
	s_cbranch_vccz .Lwb_1228p_0
	s_waitcnt vmcnt(8)

.Lwa_1228p_1:
	s_waitcnt lgkmcnt(0)
	s_barrier
	s_setprio 1
	s_waitcnt lgkmcnt(0)
	v_mfma_f32_16x16x32_bf16 v[62:65], v[146:149], v[186:189], 0
	v_mfma_f32_16x16x32_bf16 v[58:61], v[162:165], v[186:189], 0
	v_mfma_f32_16x16x32_bf16 v[46:49], v[146:149], v[194:197], 0
	v_mfma_f32_16x16x32_bf16 v[42:45], v[162:165], v[194:197], 0
	v_mfma_f32_16x16x32_bf16 v[30:33], v[146:149], v[202:205], 0
	v_mfma_f32_16x16x32_bf16 v[26:29], v[162:165], v[202:205], 0
	v_mfma_f32_16x16x32_bf16 v[14:17], v[146:149], v[210:213], 0
	v_mfma_f32_16x16x32_bf16 v[10:13], v[162:165], v[210:213], 0
	v_mfma_f32_16x16x32_bf16 v[62:65], v[158:161], v[190:193], v[62:65]
	v_mfma_f32_16x16x32_bf16 v[58:61], v[166:169], v[190:193], v[58:61]
	v_mfma_f32_16x16x32_bf16 v[46:49], v[158:161], v[198:201], v[46:49]
	v_mfma_f32_16x16x32_bf16 v[42:45], v[166:169], v[198:201], v[42:45]
	v_mfma_f32_16x16x32_bf16 v[30:33], v[158:161], v[206:209], v[30:33]
	v_mfma_f32_16x16x32_bf16 v[26:29], v[166:169], v[206:209], v[26:29]
	v_mfma_f32_16x16x32_bf16 v[14:17], v[158:161], v[214:217], v[14:17]
	v_mfma_f32_16x16x32_bf16 v[10:13], v[166:169], v[214:217], v[10:13]
	v_mfma_f32_16x16x32_bf16 v[54:57], v[170:173], v[186:189], 0
	v_mfma_f32_16x16x32_bf16 v[50:53], v[178:181], v[186:189], 0
	v_mfma_f32_16x16x32_bf16 v[38:41], v[170:173], v[194:197], 0
	v_mfma_f32_16x16x32_bf16 v[34:37], v[178:181], v[194:197], 0
	v_mfma_f32_16x16x32_bf16 v[22:25], v[170:173], v[202:205], 0
	v_mfma_f32_16x16x32_bf16 v[18:21], v[178:181], v[202:205], 0
	v_mfma_f32_16x16x32_bf16 v[6:9], v[170:173], v[210:213], 0
	v_mfma_f32_16x16x32_bf16 v[2:5], v[178:181], v[210:213], 0
	v_mfma_f32_16x16x32_bf16 v[54:57], v[174:177], v[190:193], v[54:57]
	v_mfma_f32_16x16x32_bf16 v[50:53], v[182:185], v[190:193], v[50:53]
	v_mfma_f32_16x16x32_bf16 v[38:41], v[174:177], v[198:201], v[38:41]
	v_mfma_f32_16x16x32_bf16 v[34:37], v[182:185], v[198:201], v[34:37]
	v_mfma_f32_16x16x32_bf16 v[22:25], v[174:177], v[206:209], v[22:25]
	v_mfma_f32_16x16x32_bf16 v[18:21], v[182:185], v[206:209], v[18:21]
	v_mfma_f32_16x16x32_bf16 v[6:9], v[174:177], v[214:217], v[6:9]
	v_mfma_f32_16x16x32_bf16 v[2:5], v[182:185], v[214:217], v[2:5]
	s_cbranch_vccz .Lwb_1228p_1
	s_waitcnt vmcnt(8)

.Lwa_1228l_0:
	s_waitcnt lgkmcnt(0)
	s_barrier
	s_setprio 1
	s_waitcnt lgkmcnt(0)
	v_mfma_f32_16x16x32_bf16 v[126:129], v[146:149], v[186:189], v[126:129]
	v_mfma_f32_16x16x32_bf16 v[122:125], v[162:165], v[186:189], v[122:125]
	v_mfma_f32_16x16x32_bf16 v[110:113], v[146:149], v[194:197], v[110:113]
	v_mfma_f32_16x16x32_bf16 v[106:109], v[162:165], v[194:197], v[106:109]
	v_mfma_f32_16x16x32_bf16 v[94:97], v[146:149], v[202:205], v[94:97]
	v_mfma_f32_16x16x32_bf16 v[90:93], v[162:165], v[202:205], v[90:93]
	v_mfma_f32_16x16x32_bf16 v[78:81], v[146:149], v[210:213], v[78:81]
	v_mfma_f32_16x16x32_bf16 v[74:77], v[162:165], v[210:213], v[74:77]
	v_mfma_f32_16x16x32_bf16 v[126:129], v[158:161], v[190:193], v[126:129]
	v_mfma_f32_16x16x32_bf16 v[122:125], v[166:169], v[190:193], v[122:125]
	v_mfma_f32_16x16x32_bf16 v[110:113], v[158:161], v[198:201], v[110:113]
	v_mfma_f32_16x16x32_bf16 v[106:109], v[166:169], v[198:201], v[106:109]
	v_mfma_f32_16x16x32_bf16 v[94:97], v[158:161], v[206:209], v[94:97]
	v_mfma_f32_16x16x32_bf16 v[90:93], v[166:169], v[206:209], v[90:93]
	v_mfma_f32_16x16x32_bf16 v[78:81], v[158:161], v[214:217], v[78:81]
	v_mfma_f32_16x16x32_bf16 v[74:77], v[166:169], v[214:217], v[74:77]
	v_mfma_f32_16x16x32_bf16 v[118:121], v[170:173], v[186:189], v[118:121]
	v_mfma_f32_16x16x32_bf16 v[114:117], v[178:181], v[186:189], v[114:117]
	v_mfma_f32_16x16x32_bf16 v[102:105], v[170:173], v[194:197], v[102:105]
	v_mfma_f32_16x16x32_bf16 v[98:101], v[178:181], v[194:197], v[98:101]
	v_mfma_f32_16x16x32_bf16 v[86:89], v[170:173], v[202:205], v[86:89]
	v_mfma_f32_16x16x32_bf16 v[82:85], v[178:181], v[202:205], v[82:85]
	v_mfma_f32_16x16x32_bf16 v[70:73], v[170:173], v[210:213], v[70:73]
	v_mfma_f32_16x16x32_bf16 v[66:69], v[178:181], v[210:213], v[66:69]
	v_mfma_f32_16x16x32_bf16 v[118:121], v[174:177], v[190:193], v[118:121]
	v_mfma_f32_16x16x32_bf16 v[114:117], v[182:185], v[190:193], v[114:117]
	v_mfma_f32_16x16x32_bf16 v[102:105], v[174:177], v[198:201], v[102:105]
	v_mfma_f32_16x16x32_bf16 v[98:101], v[182:185], v[198:201], v[98:101]
	v_mfma_f32_16x16x32_bf16 v[86:89], v[174:177], v[206:209], v[86:89]
	v_mfma_f32_16x16x32_bf16 v[82:85], v[182:185], v[206:209], v[82:85]
	v_mfma_f32_16x16x32_bf16 v[70:73], v[174:177], v[214:217], v[70:73]
	v_mfma_f32_16x16x32_bf16 v[66:69], v[182:185], v[214:217], v[66:69]
	s_cbranch_vccz .Lwb_1228l_0
	s_waitcnt vmcnt(8)

.Lwa_1228l_1:
	s_waitcnt lgkmcnt(0)
	s_barrier
	s_setprio 1
	s_waitcnt lgkmcnt(0)
	v_mfma_f32_16x16x32_bf16 v[62:65], v[146:149], v[186:189], v[62:65]
	v_mfma_f32_16x16x32_bf16 v[58:61], v[162:165], v[186:189], v[58:61]
	v_mfma_f32_16x16x32_bf16 v[46:49], v[146:149], v[194:197], v[46:49]
	v_mfma_f32_16x16x32_bf16 v[42:45], v[162:165], v[194:197], v[42:45]
	v_mfma_f32_16x16x32_bf16 v[30:33], v[146:149], v[202:205], v[30:33]
	v_mfma_f32_16x16x32_bf16 v[26:29], v[162:165], v[202:205], v[26:29]
	v_mfma_f32_16x16x32_bf16 v[14:17], v[146:149], v[210:213], v[14:17]
	v_mfma_f32_16x16x32_bf16 v[10:13], v[162:165], v[210:213], v[10:13]
	v_mfma_f32_16x16x32_bf16 v[62:65], v[158:161], v[190:193], v[62:65]
	v_mfma_f32_16x16x32_bf16 v[58:61], v[166:169], v[190:193], v[58:61]
	v_mfma_f32_16x16x32_bf16 v[46:49], v[158:161], v[198:201], v[46:49]
	v_mfma_f32_16x16x32_bf16 v[42:45], v[166:169], v[198:201], v[42:45]
	v_mfma_f32_16x16x32_bf16 v[30:33], v[158:161], v[206:209], v[30:33]
	v_mfma_f32_16x16x32_bf16 v[26:29], v[166:169], v[206:209], v[26:29]
	v_mfma_f32_16x16x32_bf16 v[14:17], v[158:161], v[214:217], v[14:17]
	v_mfma_f32_16x16x32_bf16 v[10:13], v[166:169], v[214:217], v[10:13]
	v_mfma_f32_16x16x32_bf16 v[54:57], v[170:173], v[186:189], v[54:57]
	v_mfma_f32_16x16x32_bf16 v[50:53], v[178:181], v[186:189], v[50:53]
	v_mfma_f32_16x16x32_bf16 v[38:41], v[170:173], v[194:197], v[38:41]
	v_mfma_f32_16x16x32_bf16 v[34:37], v[178:181], v[194:197], v[34:37]
	v_mfma_f32_16x16x32_bf16 v[22:25], v[170:173], v[202:205], v[22:25]
	v_mfma_f32_16x16x32_bf16 v[18:21], v[178:181], v[202:205], v[18:21]
	v_mfma_f32_16x16x32_bf16 v[6:9], v[170:173], v[210:213], v[6:9]
	v_mfma_f32_16x16x32_bf16 v[2:5], v[178:181], v[210:213], v[2:5]
	v_mfma_f32_16x16x32_bf16 v[54:57], v[174:177], v[190:193], v[54:57]
	v_mfma_f32_16x16x32_bf16 v[50:53], v[182:185], v[190:193], v[50:53]
	v_mfma_f32_16x16x32_bf16 v[38:41], v[174:177], v[198:201], v[38:41]
	v_mfma_f32_16x16x32_bf16 v[34:37], v[182:185], v[198:201], v[34:37]
	v_mfma_f32_16x16x32_bf16 v[22:25], v[174:177], v[206:209], v[22:25]
	v_mfma_f32_16x16x32_bf16 v[18:21], v[182:185], v[206:209], v[18:21]
	v_mfma_f32_16x16x32_bf16 v[6:9], v[174:177], v[214:217], v[6:9]
	v_mfma_f32_16x16x32_bf16 v[2:5], v[182:185], v[214:217], v[2:5]
	s_cbranch_vccz .Lwb_1228l_1
	s_waitcnt vmcnt(8)

.LBB0_1481:
	s_lshl_b32 s1, s30, 7
	s_ashr_i32 s0, s30, 4
	s_and_b32 s1, s1, 0x780
	v_or_b32_e32 v240, s1, v184
	s_ashr_i32 s1, s0, 31
	s_lshl_b64 s[0:1], s[0:1], 13
	s_add_u32 s2, s8, s0
	s_addc_u32 s3, s9, s1
	v_lshlrev_b32_e32 v240, 2, v240
	s_add_u32 s0, s10, s0
	s_addc_u32 s1, s11, s1
	global_load_dwordx4 v[224:227], v240, s[2:3]
	global_load_dwordx4 v[228:231], v240, s[2:3] offset:16
	global_load_dwordx4 v[232:235], v240, s[0:1]
	global_load_dwordx4 v[236:239], v240, s[0:1] offset:16
	s_ashr_i32 s21, s20, 31
	s_lshl_b64 s[0:1], s[20:21], 19
	s_add_u32 s24, s47, s0
	s_addc_u32 s25, s48, s1
	s_and_b64 s[0:1], s[4:5], exec
	s_cselect_b32 s21, s25, s37
	s_cselect_b32 s63, s24, s36
	s_ashr_i32 s23, s22, 31
	s_lshl_b64 s[0:1], s[22:23], 19
	s_add_u32 s26, s45, s0
	s_addc_u32 s27, s46, s1
	s_and_b64 s[0:1], s[4:5], exec
	s_cselect_b32 s23, s27, s35
	s_cselect_b32 s64, s26, s34
	s_add_u32 s65, s34, 0x4000
	s_addc_u32 s66, s35, 0
	s_add_u32 s34, s36, 0x40080
	s_addc_u32 s35, s37, 0
	s_mov_b32 s67, -2
	ds_read_b128 v[26:29], v185
	ds_read_b128 v[30:33], v185 offset:1024
	ds_read_b128 v[18:21], v185 offset:2048
	ds_read_b128 v[22:25], v185 offset:3072
	ds_read_b128 v[10:13], v186
	ds_read_b128 v[14:17], v186 offset:1024
	ds_read_b128 v[2:5], v186 offset:2048
	ds_read_b128 v[6:9], v186 offset:3072
	s_add_u32 s0, s34, 0xfffc0080
	s_addc_u32 s1, s35, -1
	s_cmp_eq_u32 s67, 12
	s_cselect_b32 s39, s21, s1
	s_cselect_b32 s38, s63, s0
	s_cselect_b32 s37, s23, s66
	s_cselect_b32 s36, s64, s65
	v_lshl_add_u64 v[178:179], s[34:35], 0, v[172:173]
	s_add_i32 m0, s29, 0xc000
	ds_read_b128 v[190:193], v187
	ds_read_b128 v[194:197], v187 offset:1024
	ds_read_b128 v[198:201], v187 offset:2048
	ds_read_b128 v[202:205], v187 offset:3072
	ds_read_b128 v[206:209], v187 offset:4096
	ds_read_b128 v[210:213], v187 offset:5120
	ds_read_b128 v[214:217], v187 offset:6144
	ds_read_b128 v[218:221], v187 offset:7168
	global_load_lds_dwordx4 v[178:179], off
	v_lshl_add_u64 v[178:179], s[34:35], 0, v[174:175]
	s_add_i32 m0, s29, 0xe000
	s_nop 0
	global_load_lds_dwordx4 v[178:179], off
	s_waitcnt vmcnt(8)
	s_waitcnt lgkmcnt(0)
	s_barrier
	s_setprio 1
	s_waitcnt lgkmcnt(0)
	v_mfma_scale_f32_16x16x128_f8f6f4 v[158:161], v[26:33], v[190:197], 0, v188, v188 op_sel_hi:[0,0,0]
	v_mfma_scale_f32_16x16x128_f8f6f4 v[154:157], v[18:25], v[190:197], 0, v188, v188 op_sel_hi:[0,0,0]
	v_mfma_scale_f32_16x16x128_f8f6f4 v[142:145], v[26:33], v[198:205], 0, v188, v188 op_sel_hi:[0,0,0]
	v_mfma_scale_f32_16x16x128_f8f6f4 v[138:141], v[18:25], v[198:205], 0, v188, v188 op_sel_hi:[0,0,0]
	v_mfma_scale_f32_16x16x128_f8f6f4 v[126:129], v[26:33], v[206:213], 0, v188, v188 op_sel_hi:[0,0,0]
	v_mfma_scale_f32_16x16x128_f8f6f4 v[122:125], v[18:25], v[206:213], 0, v188, v188 op_sel_hi:[0,0,0]
	v_mfma_scale_f32_16x16x128_f8f6f4 v[110:113], v[26:33], v[214:221], 0, v188, v188 op_sel_hi:[0,0,0]
	v_mfma_scale_f32_16x16x128_f8f6f4 v[106:109], v[18:25], v[214:221], 0, v188, v188 op_sel_hi:[0,0,0]
	v_mfma_scale_f32_16x16x128_f8f6f4 v[150:153], v[10:17], v[190:197], 0, v188, v188 op_sel_hi:[0,0,0]
	v_mfma_scale_f32_16x16x128_f8f6f4 v[146:149], v[2:9], v[190:197], 0, v188, v188 op_sel_hi:[0,0,0]
	v_mfma_scale_f32_16x16x128_f8f6f4 v[134:137], v[10:17], v[198:205], 0, v188, v188 op_sel_hi:[0,0,0]
	v_mfma_scale_f32_16x16x128_f8f6f4 v[130:133], v[2:9], v[198:205], 0, v188, v188 op_sel_hi:[0,0,0]
	v_mfma_scale_f32_16x16x128_f8f6f4 v[118:121], v[10:17], v[206:213], 0, v188, v188 op_sel_hi:[0,0,0]
	v_mfma_scale_f32_16x16x128_f8f6f4 v[114:117], v[2:9], v[206:213], 0, v188, v188 op_sel_hi:[0,0,0]
	v_mfma_scale_f32_16x16x128_f8f6f4 v[102:105], v[10:17], v[214:221], 0, v188, v188 op_sel_hi:[0,0,0]
	v_mfma_scale_f32_16x16x128_f8f6f4 v[98:101], v[2:9], v[214:221], 0, v188, v188 op_sel_hi:[0,0,0]
	s_setprio 0
	s_barrier
	s_add_i32 s0, s57, s49
	v_lshl_add_u64 v[178:179], s[36:37], 0, v[164:165]
	s_mov_b32 m0, s0
	ds_read_b128 v[190:193], v187 offset:16384
	ds_read_b128 v[194:197], v187 offset:17408
	ds_read_b128 v[198:201], v187 offset:18432
	ds_read_b128 v[202:205], v187 offset:19456
	ds_read_b128 v[206:209], v187 offset:20480
	ds_read_b128 v[210:213], v187 offset:21504
	ds_read_b128 v[214:217], v187 offset:22528
	ds_read_b128 v[218:221], v187 offset:23552
	global_load_lds_dwordx4 v[178:179], off
	s_add_i32 m0, s0, 0x2000
	s_add_u32 s0, s36, 0x40000
	v_lshl_add_u64 v[178:179], s[36:37], 0, v[168:169]
	s_addc_u32 s1, s37, 0
	s_add_i32 s2, s58, s49
	global_load_lds_dwordx4 v[178:179], off
	v_lshl_add_u64 v[178:179], s[0:1], 0, v[164:165]
	s_mov_b32 m0, s2
	v_lshl_add_u64 v[180:181], s[38:39], 0, v[166:167]
	global_load_lds_dwordx4 v[178:179], off
	v_lshl_add_u64 v[178:179], s[0:1], 0, v[168:169]
	s_add_i32 m0, s2, 0x2000
	s_nop 0
	global_load_lds_dwordx4 v[178:179], off
	v_lshl_add_u64 v[178:179], s[38:39], 0, v[162:163]
	s_mov_b32 m0, s29
	s_nop 0
	global_load_lds_dwordx4 v[178:179], off
	s_mov_b32 m0, s31
	s_nop 0
	global_load_lds_dwordx4 v[180:181], off
	s_waitcnt vmcnt(8)
	s_waitcnt lgkmcnt(0)
	s_barrier
	s_setprio 1
	s_waitcnt lgkmcnt(0)
	v_mfma_scale_f32_16x16x128_f8f6f4 v[94:97], v[26:33], v[190:197], 0, v188, v188 op_sel_hi:[0,0,0]
	v_mfma_scale_f32_16x16x128_f8f6f4 v[90:93], v[18:25], v[190:197], 0, v188, v188 op_sel_hi:[0,0,0]
	v_mfma_scale_f32_16x16x128_f8f6f4 v[78:81], v[26:33], v[198:205], 0, v188, v188 op_sel_hi:[0,0,0]
	v_mfma_scale_f32_16x16x128_f8f6f4 v[74:77], v[18:25], v[198:205], 0, v188, v188 op_sel_hi:[0,0,0]
	v_mfma_scale_f32_16x16x128_f8f6f4 v[62:65], v[26:33], v[206:213], 0, v188, v188 op_sel_hi:[0,0,0]
	v_mfma_scale_f32_16x16x128_f8f6f4 v[58:61], v[18:25], v[206:213], 0, v188, v188 op_sel_hi:[0,0,0]
	v_mfma_scale_f32_16x16x128_f8f6f4 v[46:49], v[26:33], v[214:221], 0, v188, v188 op_sel_hi:[0,0,0]
	v_mfma_scale_f32_16x16x128_f8f6f4 v[42:45], v[18:25], v[214:221], 0, v188, v188 op_sel_hi:[0,0,0]
	v_mfma_scale_f32_16x16x128_f8f6f4 v[86:89], v[10:17], v[190:197], 0, v188, v188 op_sel_hi:[0,0,0]
	v_mfma_scale_f32_16x16x128_f8f6f4 v[82:85], v[2:9], v[190:197], 0, v188, v188 op_sel_hi:[0,0,0]
	v_mfma_scale_f32_16x16x128_f8f6f4 v[70:73], v[10:17], v[198:205], 0, v188, v188 op_sel_hi:[0,0,0]
	v_mfma_scale_f32_16x16x128_f8f6f4 v[66:69], v[2:9], v[198:205], 0, v188, v188 op_sel_hi:[0,0,0]
	v_mfma_scale_f32_16x16x128_f8f6f4 v[54:57], v[10:17], v[206:213], 0, v188, v188 op_sel_hi:[0,0,0]
	v_mfma_scale_f32_16x16x128_f8f6f4 v[50:53], v[2:9], v[206:213], 0, v188, v188 op_sel_hi:[0,0,0]
	v_mfma_scale_f32_16x16x128_f8f6f4 v[38:41], v[10:17], v[214:221], 0, v188, v188 op_sel_hi:[0,0,0]
	v_mfma_scale_f32_16x16x128_f8f6f4 v[34:37], v[2:9], v[214:221], 0, v188, v188 op_sel_hi:[0,0,0]
	s_setprio 0
	s_barrier
	s_branch .Lmid_1482
.LBB0_1482:
	ds_read_b128 v[26:29], v185
	ds_read_b128 v[30:33], v185 offset:1024
	ds_read_b128 v[18:21], v185 offset:2048
	ds_read_b128 v[22:25], v185 offset:3072
	ds_read_b128 v[10:13], v186
	ds_read_b128 v[14:17], v186 offset:1024
	ds_read_b128 v[2:5], v186 offset:2048
	ds_read_b128 v[6:9], v186 offset:3072
	s_add_u32 s0, s34, 0xfffc0080
	s_addc_u32 s1, s35, -1
	s_cmp_eq_u32 s67, 12
	s_cselect_b32 s39, s21, s1
	s_cselect_b32 s38, s63, s0
	s_cselect_b32 s37, s23, s66
	s_cselect_b32 s36, s64, s65
	v_lshl_add_u64 v[178:179], s[34:35], 0, v[172:173]
	s_add_i32 m0, s29, 0xc000
	ds_read_b128 v[190:193], v187
	ds_read_b128 v[194:197], v187 offset:1024
	ds_read_b128 v[198:201], v187 offset:2048
	ds_read_b128 v[202:205], v187 offset:3072
	ds_read_b128 v[206:209], v187 offset:4096
	ds_read_b128 v[210:213], v187 offset:5120
	ds_read_b128 v[214:217], v187 offset:6144
	ds_read_b128 v[218:221], v187 offset:7168
	global_load_lds_dwordx4 v[178:179], off
	v_lshl_add_u64 v[178:179], s[34:35], 0, v[174:175]
	s_add_i32 m0, s29, 0xe000
	s_nop 0
	global_load_lds_dwordx4 v[178:179], off
	s_waitcnt vmcnt(8)
	s_waitcnt lgkmcnt(0)
	s_barrier
	s_setprio 1
	s_waitcnt lgkmcnt(0)
	v_mfma_scale_f32_16x16x128_f8f6f4 v[158:161], v[26:33], v[190:197], v[158:161], v188, v188 op_sel_hi:[0,0,0]
	v_mfma_scale_f32_16x16x128_f8f6f4 v[154:157], v[18:25], v[190:197], v[154:157], v188, v188 op_sel_hi:[0,0,0]
	v_mfma_scale_f32_16x16x128_f8f6f4 v[142:145], v[26:33], v[198:205], v[142:145], v188, v188 op_sel_hi:[0,0,0]
	v_mfma_scale_f32_16x16x128_f8f6f4 v[138:141], v[18:25], v[198:205], v[138:141], v188, v188 op_sel_hi:[0,0,0]
	v_mfma_scale_f32_16x16x128_f8f6f4 v[126:129], v[26:33], v[206:213], v[126:129], v188, v188 op_sel_hi:[0,0,0]
	v_mfma_scale_f32_16x16x128_f8f6f4 v[122:125], v[18:25], v[206:213], v[122:125], v188, v188 op_sel_hi:[0,0,0]
	v_mfma_scale_f32_16x16x128_f8f6f4 v[110:113], v[26:33], v[214:221], v[110:113], v188, v188 op_sel_hi:[0,0,0]
	v_mfma_scale_f32_16x16x128_f8f6f4 v[106:109], v[18:25], v[214:221], v[106:109], v188, v188 op_sel_hi:[0,0,0]
	v_mfma_scale_f32_16x16x128_f8f6f4 v[150:153], v[10:17], v[190:197], v[150:153], v188, v188 op_sel_hi:[0,0,0]
	v_mfma_scale_f32_16x16x128_f8f6f4 v[146:149], v[2:9], v[190:197], v[146:149], v188, v188 op_sel_hi:[0,0,0]
	v_mfma_scale_f32_16x16x128_f8f6f4 v[134:137], v[10:17], v[198:205], v[134:137], v188, v188 op_sel_hi:[0,0,0]
	v_mfma_scale_f32_16x16x128_f8f6f4 v[130:133], v[2:9], v[198:205], v[130:133], v188, v188 op_sel_hi:[0,0,0]
	v_mfma_scale_f32_16x16x128_f8f6f4 v[118:121], v[10:17], v[206:213], v[118:121], v188, v188 op_sel_hi:[0,0,0]
	v_mfma_scale_f32_16x16x128_f8f6f4 v[114:117], v[2:9], v[206:213], v[114:117], v188, v188 op_sel_hi:[0,0,0]
	v_mfma_scale_f32_16x16x128_f8f6f4 v[102:105], v[10:17], v[214:221], v[102:105], v188, v188 op_sel_hi:[0,0,0]
	v_mfma_scale_f32_16x16x128_f8f6f4 v[98:101], v[2:9], v[214:221], v[98:101], v188, v188 op_sel_hi:[0,0,0]
	s_setprio 0
	s_barrier
	s_add_i32 s0, s57, s49
	v_lshl_add_u64 v[178:179], s[36:37], 0, v[164:165]
	s_mov_b32 m0, s0
	ds_read_b128 v[190:193], v187 offset:16384
	ds_read_b128 v[194:197], v187 offset:17408
	ds_read_b128 v[198:201], v187 offset:18432
	ds_read_b128 v[202:205], v187 offset:19456
	ds_read_b128 v[206:209], v187 offset:20480
	ds_read_b128 v[210:213], v187 offset:21504
	ds_read_b128 v[214:217], v187 offset:22528
	ds_read_b128 v[218:221], v187 offset:23552
	global_load_lds_dwordx4 v[178:179], off
	s_add_i32 m0, s0, 0x2000
	s_add_u32 s0, s36, 0x40000
	v_lshl_add_u64 v[178:179], s[36:37], 0, v[168:169]
	s_addc_u32 s1, s37, 0
	s_add_i32 s2, s58, s49
	global_load_lds_dwordx4 v[178:179], off
	v_lshl_add_u64 v[178:179], s[0:1], 0, v[164:165]
	s_mov_b32 m0, s2
	v_lshl_add_u64 v[180:181], s[38:39], 0, v[166:167]
	global_load_lds_dwordx4 v[178:179], off
	v_lshl_add_u64 v[178:179], s[0:1], 0, v[168:169]
	s_add_i32 m0, s2, 0x2000
	s_nop 0
	global_load_lds_dwordx4 v[178:179], off
	v_lshl_add_u64 v[178:179], s[38:39], 0, v[162:163]
	s_mov_b32 m0, s29
	s_nop 0
	global_load_lds_dwordx4 v[178:179], off
	s_mov_b32 m0, s31
	s_nop 0
	global_load_lds_dwordx4 v[180:181], off
	s_waitcnt vmcnt(8)
	s_waitcnt lgkmcnt(0)
	s_barrier
	s_setprio 1
	s_waitcnt lgkmcnt(0)
	v_mfma_scale_f32_16x16x128_f8f6f4 v[94:97], v[26:33], v[190:197], v[94:97], v188, v188 op_sel_hi:[0,0,0]
	v_mfma_scale_f32_16x16x128_f8f6f4 v[90:93], v[18:25], v[190:197], v[90:93], v188, v188 op_sel_hi:[0,0,0]
	v_mfma_scale_f32_16x16x128_f8f6f4 v[78:81], v[26:33], v[198:205], v[78:81], v188, v188 op_sel_hi:[0,0,0]
	v_mfma_scale_f32_16x16x128_f8f6f4 v[74:77], v[18:25], v[198:205], v[74:77], v188, v188 op_sel_hi:[0,0,0]
	v_mfma_scale_f32_16x16x128_f8f6f4 v[62:65], v[26:33], v[206:213], v[62:65], v188, v188 op_sel_hi:[0,0,0]
	v_mfma_scale_f32_16x16x128_f8f6f4 v[58:61], v[18:25], v[206:213], v[58:61], v188, v188 op_sel_hi:[0,0,0]
	v_mfma_scale_f32_16x16x128_f8f6f4 v[46:49], v[26:33], v[214:221], v[46:49], v188, v188 op_sel_hi:[0,0,0]
	v_mfma_scale_f32_16x16x128_f8f6f4 v[42:45], v[18:25], v[214:221], v[42:45], v188, v188 op_sel_hi:[0,0,0]
	v_mfma_scale_f32_16x16x128_f8f6f4 v[86:89], v[10:17], v[190:197], v[86:89], v188, v188 op_sel_hi:[0,0,0]
	v_mfma_scale_f32_16x16x128_f8f6f4 v[82:85], v[2:9], v[190:197], v[82:85], v188, v188 op_sel_hi:[0,0,0]
	v_mfma_scale_f32_16x16x128_f8f6f4 v[70:73], v[10:17], v[198:205], v[70:73], v188, v188 op_sel_hi:[0,0,0]
	v_mfma_scale_f32_16x16x128_f8f6f4 v[66:69], v[2:9], v[198:205], v[66:69], v188, v188 op_sel_hi:[0,0,0]
	v_mfma_scale_f32_16x16x128_f8f6f4 v[54:57], v[10:17], v[206:213], v[54:57], v188, v188 op_sel_hi:[0,0,0]
	v_mfma_scale_f32_16x16x128_f8f6f4 v[50:53], v[2:9], v[206:213], v[50:53], v188, v188 op_sel_hi:[0,0,0]
	v_mfma_scale_f32_16x16x128_f8f6f4 v[38:41], v[10:17], v[214:221], v[38:41], v188, v188 op_sel_hi:[0,0,0]
	v_mfma_scale_f32_16x16x128_f8f6f4 v[34:37], v[2:9], v[214:221], v[34:37], v188, v188 op_sel_hi:[0,0,0]
	s_setprio 0
	s_barrier
.Lmid_1482:
	s_add_i32 s2, 0, 0x18000
	v_add_u32_e32 v0, s2, v183
	s_add_i32 s3, 0, 0x1c000
	ds_read_b128 v[2:5], v0
	ds_read_b128 v[6:9], v0 offset:1024
	ds_read_b128 v[10:13], v0 offset:2048
	ds_read_b128 v[14:17], v0 offset:3072
	v_add_u32_e32 v0, s3, v183
	ds_read_b128 v[18:21], v0
	ds_read_b128 v[22:25], v0 offset:1024
	ds_read_b128 v[26:29], v0 offset:2048
	ds_read_b128 v[30:33], v0 offset:3072
	s_add_u32 s0, s38, 0x40000
	s_addc_u32 s1, s39, 0
	s_mov_b32 m0, s50
	v_lshl_add_u64 v[222:223], s[0:1], 0, v[162:163]
	ds_read_b128 v[190:193], v187 offset:32768
	ds_read_b128 v[194:197], v187 offset:33792
	ds_read_b128 v[198:201], v187 offset:34816
	ds_read_b128 v[202:205], v187 offset:35840
	ds_read_b128 v[206:209], v187 offset:36864
	ds_read_b128 v[210:213], v187 offset:37888
	ds_read_b128 v[214:217], v187 offset:38912
	ds_read_b128 v[218:221], v187 offset:39936
	global_load_lds_dwordx4 v[222:223], off
	v_lshl_add_u64 v[222:223], s[0:1], 0, v[166:167]
	s_mov_b32 m0, s51
	s_nop 0
	global_load_lds_dwordx4 v[222:223], off
	s_waitcnt vmcnt(8)
	s_waitcnt lgkmcnt(0)
	s_barrier
	s_setprio 1
	s_waitcnt lgkmcnt(0)
	v_mfma_scale_f32_16x16x128_f8f6f4 v[158:161], v[2:9], v[190:197], v[158:161], v188, v188 op_sel_hi:[0,0,0]
	v_mfma_scale_f32_16x16x128_f8f6f4 v[154:157], v[10:17], v[190:197], v[154:157], v188, v188 op_sel_hi:[0,0,0]
	v_mfma_scale_f32_16x16x128_f8f6f4 v[142:145], v[2:9], v[198:205], v[142:145], v188, v188 op_sel_hi:[0,0,0]
	v_mfma_scale_f32_16x16x128_f8f6f4 v[138:141], v[10:17], v[198:205], v[138:141], v188, v188 op_sel_hi:[0,0,0]
	v_mfma_scale_f32_16x16x128_f8f6f4 v[126:129], v[2:9], v[206:213], v[126:129], v188, v188 op_sel_hi:[0,0,0]
	v_mfma_scale_f32_16x16x128_f8f6f4 v[122:125], v[10:17], v[206:213], v[122:125], v188, v188 op_sel_hi:[0,0,0]
	v_mfma_scale_f32_16x16x128_f8f6f4 v[110:113], v[2:9], v[214:221], v[110:113], v188, v188 op_sel_hi:[0,0,0]
	v_mfma_scale_f32_16x16x128_f8f6f4 v[106:109], v[10:17], v[214:221], v[106:109], v188, v188 op_sel_hi:[0,0,0]
	v_mfma_scale_f32_16x16x128_f8f6f4 v[150:153], v[18:25], v[190:197], v[150:153], v188, v188 op_sel_hi:[0,0,0]
	v_mfma_scale_f32_16x16x128_f8f6f4 v[146:149], v[26:33], v[190:197], v[146:149], v188, v188 op_sel_hi:[0,0,0]
	v_mfma_scale_f32_16x16x128_f8f6f4 v[134:137], v[18:25], v[198:205], v[134:137], v188, v188 op_sel_hi:[0,0,0]
	v_mfma_scale_f32_16x16x128_f8f6f4 v[130:133], v[26:33], v[198:205], v[130:133], v188, v188 op_sel_hi:[0,0,0]
	v_mfma_scale_f32_16x16x128_f8f6f4 v[118:121], v[18:25], v[206:213], v[118:121], v188, v188 op_sel_hi:[0,0,0]
	v_mfma_scale_f32_16x16x128_f8f6f4 v[114:117], v[26:33], v[206:213], v[114:117], v188, v188 op_sel_hi:[0,0,0]
	v_mfma_scale_f32_16x16x128_f8f6f4 v[102:105], v[18:25], v[214:221], v[102:105], v188, v188 op_sel_hi:[0,0,0]
	v_mfma_scale_f32_16x16x128_f8f6f4 v[98:101], v[26:33], v[214:221], v[98:101], v188, v188 op_sel_hi:[0,0,0]
	s_setprio 0
	s_barrier
	s_add_u32 s0, s36, 0x2000
	s_addc_u32 s1, s37, 0
	s_add_i32 s2, s2, s49
	v_lshl_add_u64 v[222:223], s[0:1], 0, v[164:165]
	s_mov_b32 m0, s2
	ds_read_b128 v[190:193], v187 offset:49152
	ds_read_b128 v[194:197], v187 offset:50176
	ds_read_b128 v[198:201], v187 offset:51200
	ds_read_b128 v[202:205], v187 offset:52224
	ds_read_b128 v[206:209], v187 offset:53248
	ds_read_b128 v[210:213], v187 offset:54272
	ds_read_b128 v[214:217], v187 offset:55296
	ds_read_b128 v[218:221], v187 offset:56320
	global_load_lds_dwordx4 v[222:223], off
	s_add_i32 m0, s2, 0x2000
	v_lshl_add_u64 v[222:223], s[0:1], 0, v[168:169]
	s_add_u32 s0, s36, 0x42000
	s_addc_u32 s1, s37, 0
	s_add_i32 s2, s3, s49
	global_load_lds_dwordx4 v[222:223], off
	v_lshl_add_u64 v[222:223], s[0:1], 0, v[164:165]
	s_mov_b32 m0, s2
	v_lshl_add_u64 v[178:179], v[178:179], 0, s[16:17]
	global_load_lds_dwordx4 v[222:223], off
	v_lshl_add_u64 v[222:223], s[0:1], 0, v[168:169]
	s_add_i32 m0, s2, 0x2000
	s_nop 0
	global_load_lds_dwordx4 v[222:223], off
	s_mov_b32 m0, s53
	s_nop 0
	global_load_lds_dwordx4 v[178:179], off
	v_lshl_add_u64 v[178:179], v[180:181], 0, s[16:17]
	s_mov_b32 m0, s54
	s_nop 0
	global_load_lds_dwordx4 v[178:179], off
	s_waitcnt vmcnt(8)
	s_waitcnt lgkmcnt(0)
	s_barrier
	s_setprio 1
	s_waitcnt lgkmcnt(0)
	v_mfma_scale_f32_16x16x128_f8f6f4 v[94:97], v[2:9], v[190:197], v[94:97], v188, v188 op_sel_hi:[0,0,0]
	v_mfma_scale_f32_16x16x128_f8f6f4 v[90:93], v[10:17], v[190:197], v[90:93], v188, v188 op_sel_hi:[0,0,0]
	v_mfma_scale_f32_16x16x128_f8f6f4 v[78:81], v[2:9], v[198:205], v[78:81], v188, v188 op_sel_hi:[0,0,0]
	v_mfma_scale_f32_16x16x128_f8f6f4 v[74:77], v[10:17], v[198:205], v[74:77], v188, v188 op_sel_hi:[0,0,0]
	v_mfma_scale_f32_16x16x128_f8f6f4 v[62:65], v[2:9], v[206:213], v[62:65], v188, v188 op_sel_hi:[0,0,0]
	v_mfma_scale_f32_16x16x128_f8f6f4 v[58:61], v[10:17], v[206:213], v[58:61], v188, v188 op_sel_hi:[0,0,0]
	v_mfma_scale_f32_16x16x128_f8f6f4 v[46:49], v[2:9], v[214:221], v[46:49], v188, v188 op_sel_hi:[0,0,0]
	v_mfma_scale_f32_16x16x128_f8f6f4 v[42:45], v[10:17], v[214:221], v[42:45], v188, v188 op_sel_hi:[0,0,0]
	v_mfma_scale_f32_16x16x128_f8f6f4 v[86:89], v[18:25], v[190:197], v[86:89], v188, v188 op_sel_hi:[0,0,0]
	v_mfma_scale_f32_16x16x128_f8f6f4 v[82:85], v[26:33], v[190:197], v[82:85], v188, v188 op_sel_hi:[0,0,0]
	v_mfma_scale_f32_16x16x128_f8f6f4 v[70:73], v[18:25], v[198:205], v[70:73], v188, v188 op_sel_hi:[0,0,0]
	v_mfma_scale_f32_16x16x128_f8f6f4 v[66:69], v[26:33], v[198:205], v[66:69], v188, v188 op_sel_hi:[0,0,0]
	v_mfma_scale_f32_16x16x128_f8f6f4 v[54:57], v[18:25], v[206:213], v[54:57], v188, v188 op_sel_hi:[0,0,0]
	v_mfma_scale_f32_16x16x128_f8f6f4 v[50:53], v[26:33], v[206:213], v[50:53], v188, v188 op_sel_hi:[0,0,0]
	v_mfma_scale_f32_16x16x128_f8f6f4 v[38:41], v[18:25], v[214:221], v[38:41], v188, v188 op_sel_hi:[0,0,0]
	v_mfma_scale_f32_16x16x128_f8f6f4 v[34:37], v[26:33], v[214:221], v[34:37], v188, v188 op_sel_hi:[0,0,0]
	s_setprio 0
	s_barrier
	s_add_i32 s67, s67, 2
	s_add_u32 s65, s65, 0x4000
	s_addc_u32 s66, s66, 0
	s_add_u32 s34, s34, 0x100
	s_addc_u32 s35, s35, 0
	s_cmp_gt_u32 s67, 13
	s_cbranch_scc0 .LBB0_1482
	s_and_b64 vcc, exec, s[18:19]
	s_cbranch_vccz .LBB0_1485
	s_barrier

.LBB0_1576:
	s_lshl_b32 s1, s38, 8
	s_ashr_i32 s0, s38, 3
	s_and_b32 s1, s1, 0x700
	v_or_b32_e32 v240, s1, v183
	s_ashr_i32 s1, s0, 31
	s_lshl_b64 s[0:1], s[0:1], 13
	s_add_u32 s2, s6, s0
	s_addc_u32 s3, s7, s1
	v_lshlrev_b32_e32 v240, 2, v240
	global_load_dwordx4 v[224:227], v240, s[2:3]
	global_load_dwordx4 v[228:231], v240, s[2:3] offset:16
	global_load_dwordx4 v[232:235], v240, s[2:3] offset:512
	global_load_dwordx4 v[236:239], v240, s[2:3] offset:528
	s_ashr_i32 s27, s26, 31
	s_lshl_b64 s[0:1], s[26:27], 19
	s_add_u32 s30, s49, s0
	s_addc_u32 s31, s50, s1
	s_and_b64 s[0:1], s[4:5], exec
	s_cselect_b32 s27, s31, s43
	s_cselect_b32 s39, s30, s42
	s_ashr_i32 s29, s28, 31
	s_lshl_b64 s[0:1], s[28:29], 19
	s_add_u32 s34, s51, s0
	s_addc_u32 s35, s52, s1
	s_and_b64 s[0:1], s[4:5], exec
	s_cselect_b32 s29, s35, s41
	s_cselect_b32 s68, s34, s40
	s_add_u32 s69, s40, 0x4000
	s_addc_u32 s70, s41, 0
	s_add_u32 s40, s42, 0x40080
	s_addc_u32 s41, s43, 0
	s_mov_b32 s71, -2
	ds_read_b128 v[26:29], v184
	ds_read_b128 v[30:33], v184 offset:1024
	ds_read_b128 v[18:21], v184 offset:2048
	ds_read_b128 v[22:25], v184 offset:3072
	ds_read_b128 v[10:13], v185
	ds_read_b128 v[14:17], v185 offset:1024
	ds_read_b128 v[2:5], v185 offset:2048
	ds_read_b128 v[6:9], v185 offset:3072
	s_add_u32 s0, s40, 0xfffc0080
	s_addc_u32 s1, s41, -1
	s_cmp_eq_u32 s71, 12
	s_cselect_b32 s45, s27, s1
	s_cselect_b32 s44, s39, s0
	s_cselect_b32 s43, s29, s70
	s_cselect_b32 s42, s68, s69
	v_lshl_add_u64 v[178:179], s[40:41], 0, v[172:173]
	s_add_i32 m0, s37, 0xc000
	ds_read_b128 v[188:191], v186
	ds_read_b128 v[192:195], v186 offset:1024
	ds_read_b128 v[196:199], v186 offset:2048
	ds_read_b128 v[200:203], v186 offset:3072
	ds_read_b128 v[204:207], v186 offset:4096
	ds_read_b128 v[208:211], v186 offset:5120
	ds_read_b128 v[212:215], v186 offset:6144
	ds_read_b128 v[216:219], v186 offset:7168
	global_load_lds_dwordx4 v[178:179], off
	v_lshl_add_u64 v[178:179], s[40:41], 0, v[174:175]
	s_add_i32 m0, s37, 0xe000
	s_nop 0
	global_load_lds_dwordx4 v[178:179], off
	s_waitcnt vmcnt(8)
	s_waitcnt lgkmcnt(0)
	s_barrier
	s_setprio 1
	s_waitcnt lgkmcnt(0)
	v_mfma_scale_f32_16x16x128_f8f6f4 v[158:161], v[26:33], v[188:195], 0, v187, v187 op_sel_hi:[0,0,0]
	v_mfma_scale_f32_16x16x128_f8f6f4 v[154:157], v[18:25], v[188:195], 0, v187, v187 op_sel_hi:[0,0,0]
	v_mfma_scale_f32_16x16x128_f8f6f4 v[150:153], v[26:33], v[196:203], 0, v187, v187 op_sel_hi:[0,0,0]
	v_mfma_scale_f32_16x16x128_f8f6f4 v[146:149], v[18:25], v[196:203], 0, v187, v187 op_sel_hi:[0,0,0]
	v_mfma_scale_f32_16x16x128_f8f6f4 v[142:145], v[26:33], v[204:211], 0, v187, v187 op_sel_hi:[0,0,0]
	v_mfma_scale_f32_16x16x128_f8f6f4 v[138:141], v[18:25], v[204:211], 0, v187, v187 op_sel_hi:[0,0,0]
	v_mfma_scale_f32_16x16x128_f8f6f4 v[134:137], v[26:33], v[212:219], 0, v187, v187 op_sel_hi:[0,0,0]
	v_mfma_scale_f32_16x16x128_f8f6f4 v[130:133], v[18:25], v[212:219], 0, v187, v187 op_sel_hi:[0,0,0]
	v_mfma_scale_f32_16x16x128_f8f6f4 v[102:105], v[10:17], v[188:195], 0, v187, v187 op_sel_hi:[0,0,0]
	v_mfma_scale_f32_16x16x128_f8f6f4 v[98:101], v[2:9], v[188:195], 0, v187, v187 op_sel_hi:[0,0,0]
	v_mfma_scale_f32_16x16x128_f8f6f4 v[86:89], v[10:17], v[196:203], 0, v187, v187 op_sel_hi:[0,0,0]
	v_mfma_scale_f32_16x16x128_f8f6f4 v[82:85], v[2:9], v[196:203], 0, v187, v187 op_sel_hi:[0,0,0]
	v_mfma_scale_f32_16x16x128_f8f6f4 v[78:81], v[10:17], v[204:211], 0, v187, v187 op_sel_hi:[0,0,0]
	v_mfma_scale_f32_16x16x128_f8f6f4 v[74:77], v[2:9], v[204:211], 0, v187, v187 op_sel_hi:[0,0,0]
	v_mfma_scale_f32_16x16x128_f8f6f4 v[70:73], v[10:17], v[212:219], 0, v187, v187 op_sel_hi:[0,0,0]
	v_mfma_scale_f32_16x16x128_f8f6f4 v[66:69], v[2:9], v[212:219], 0, v187, v187 op_sel_hi:[0,0,0]
	s_setprio 0
	s_barrier
	s_add_i32 s0, s62, s53
	v_lshl_add_u64 v[178:179], s[42:43], 0, v[164:165]
	s_mov_b32 m0, s0
	ds_read_b128 v[188:191], v186 offset:16384
	ds_read_b128 v[192:195], v186 offset:17408
	ds_read_b128 v[196:199], v186 offset:18432
	ds_read_b128 v[200:203], v186 offset:19456
	ds_read_b128 v[204:207], v186 offset:20480
	ds_read_b128 v[208:211], v186 offset:21504
	ds_read_b128 v[212:215], v186 offset:22528
	ds_read_b128 v[216:219], v186 offset:23552
	global_load_lds_dwordx4 v[178:179], off
	s_add_i32 m0, s0, 0x2000
	s_add_u32 s0, s42, 0x40000
	v_lshl_add_u64 v[178:179], s[42:43], 0, v[168:169]
	s_addc_u32 s1, s43, 0
	s_add_i32 s2, s63, s53
	global_load_lds_dwordx4 v[178:179], off
	v_lshl_add_u64 v[178:179], s[0:1], 0, v[164:165]
	s_mov_b32 m0, s2
	v_lshl_add_u64 v[180:181], s[44:45], 0, v[166:167]
	global_load_lds_dwordx4 v[178:179], off
	v_lshl_add_u64 v[178:179], s[0:1], 0, v[168:169]
	s_add_i32 m0, s2, 0x2000
	s_nop 0
	global_load_lds_dwordx4 v[178:179], off
	v_lshl_add_u64 v[178:179], s[44:45], 0, v[162:163]
	s_mov_b32 m0, s37
	s_nop 0
	global_load_lds_dwordx4 v[178:179], off
	s_mov_b32 m0, s54
	s_nop 0
	global_load_lds_dwordx4 v[180:181], off
	s_waitcnt vmcnt(8)
	s_waitcnt lgkmcnt(0)
	s_barrier
	s_setprio 1
	s_waitcnt lgkmcnt(0)
	v_mfma_scale_f32_16x16x128_f8f6f4 v[126:129], v[26:33], v[188:195], 0, v187, v187 op_sel_hi:[0,0,0]
	v_mfma_scale_f32_16x16x128_f8f6f4 v[122:125], v[18:25], v[188:195], 0, v187, v187 op_sel_hi:[0,0,0]
	v_mfma_scale_f32_16x16x128_f8f6f4 v[118:121], v[26:33], v[196:203], 0, v187, v187 op_sel_hi:[0,0,0]
	v_mfma_scale_f32_16x16x128_f8f6f4 v[114:117], v[18:25], v[196:203], 0, v187, v187 op_sel_hi:[0,0,0]
	v_mfma_scale_f32_16x16x128_f8f6f4 v[110:113], v[26:33], v[204:211], 0, v187, v187 op_sel_hi:[0,0,0]
	v_mfma_scale_f32_16x16x128_f8f6f4 v[106:109], v[18:25], v[204:211], 0, v187, v187 op_sel_hi:[0,0,0]
	v_mfma_scale_f32_16x16x128_f8f6f4 v[94:97], v[26:33], v[212:219], 0, v187, v187 op_sel_hi:[0,0,0]
	v_mfma_scale_f32_16x16x128_f8f6f4 v[90:93], v[18:25], v[212:219], 0, v187, v187 op_sel_hi:[0,0,0]
	v_mfma_scale_f32_16x16x128_f8f6f4 v[62:65], v[10:17], v[188:195], 0, v187, v187 op_sel_hi:[0,0,0]
	v_mfma_scale_f32_16x16x128_f8f6f4 v[58:61], v[2:9], v[188:195], 0, v187, v187 op_sel_hi:[0,0,0]
	v_mfma_scale_f32_16x16x128_f8f6f4 v[54:57], v[10:17], v[196:203], 0, v187, v187 op_sel_hi:[0,0,0]
	v_mfma_scale_f32_16x16x128_f8f6f4 v[50:53], v[2:9], v[196:203], 0, v187, v187 op_sel_hi:[0,0,0]
	v_mfma_scale_f32_16x16x128_f8f6f4 v[46:49], v[10:17], v[204:211], 0, v187, v187 op_sel_hi:[0,0,0]
	v_mfma_scale_f32_16x16x128_f8f6f4 v[42:45], v[2:9], v[204:211], 0, v187, v187 op_sel_hi:[0,0,0]
	v_mfma_scale_f32_16x16x128_f8f6f4 v[38:41], v[10:17], v[212:219], 0, v187, v187 op_sel_hi:[0,0,0]
	v_mfma_scale_f32_16x16x128_f8f6f4 v[34:37], v[2:9], v[212:219], 0, v187, v187 op_sel_hi:[0,0,0]
	s_setprio 0
	s_barrier
	s_branch .Lmid_1577
.LBB0_1577:
	ds_read_b128 v[26:29], v184
	ds_read_b128 v[30:33], v184 offset:1024
	ds_read_b128 v[18:21], v184 offset:2048
	ds_read_b128 v[22:25], v184 offset:3072
	ds_read_b128 v[10:13], v185
	ds_read_b128 v[14:17], v185 offset:1024
	ds_read_b128 v[2:5], v185 offset:2048
	ds_read_b128 v[6:9], v185 offset:3072
	s_add_u32 s0, s40, 0xfffc0080
	s_addc_u32 s1, s41, -1
	s_cmp_eq_u32 s71, 12
	s_cselect_b32 s45, s27, s1
	s_cselect_b32 s44, s39, s0
	s_cselect_b32 s43, s29, s70
	s_cselect_b32 s42, s68, s69
	v_lshl_add_u64 v[178:179], s[40:41], 0, v[172:173]
	s_add_i32 m0, s37, 0xc000
	ds_read_b128 v[188:191], v186
	ds_read_b128 v[192:195], v186 offset:1024
	ds_read_b128 v[196:199], v186 offset:2048
	ds_read_b128 v[200:203], v186 offset:3072
	ds_read_b128 v[204:207], v186 offset:4096
	ds_read_b128 v[208:211], v186 offset:5120
	ds_read_b128 v[212:215], v186 offset:6144
	ds_read_b128 v[216:219], v186 offset:7168
	global_load_lds_dwordx4 v[178:179], off
	v_lshl_add_u64 v[178:179], s[40:41], 0, v[174:175]
	s_add_i32 m0, s37, 0xe000
	s_nop 0
	global_load_lds_dwordx4 v[178:179], off
	s_waitcnt vmcnt(8)
	s_waitcnt lgkmcnt(0)
	s_barrier
	s_setprio 1
	s_waitcnt lgkmcnt(0)
	v_mfma_scale_f32_16x16x128_f8f6f4 v[158:161], v[26:33], v[188:195], v[158:161], v187, v187 op_sel_hi:[0,0,0]
	v_mfma_scale_f32_16x16x128_f8f6f4 v[154:157], v[18:25], v[188:195], v[154:157], v187, v187 op_sel_hi:[0,0,0]
	v_mfma_scale_f32_16x16x128_f8f6f4 v[150:153], v[26:33], v[196:203], v[150:153], v187, v187 op_sel_hi:[0,0,0]
	v_mfma_scale_f32_16x16x128_f8f6f4 v[146:149], v[18:25], v[196:203], v[146:149], v187, v187 op_sel_hi:[0,0,0]
	v_mfma_scale_f32_16x16x128_f8f6f4 v[142:145], v[26:33], v[204:211], v[142:145], v187, v187 op_sel_hi:[0,0,0]
	v_mfma_scale_f32_16x16x128_f8f6f4 v[138:141], v[18:25], v[204:211], v[138:141], v187, v187 op_sel_hi:[0,0,0]
	v_mfma_scale_f32_16x16x128_f8f6f4 v[134:137], v[26:33], v[212:219], v[134:137], v187, v187 op_sel_hi:[0,0,0]
	v_mfma_scale_f32_16x16x128_f8f6f4 v[130:133], v[18:25], v[212:219], v[130:133], v187, v187 op_sel_hi:[0,0,0]
	v_mfma_scale_f32_16x16x128_f8f6f4 v[102:105], v[10:17], v[188:195], v[102:105], v187, v187 op_sel_hi:[0,0,0]
	v_mfma_scale_f32_16x16x128_f8f6f4 v[98:101], v[2:9], v[188:195], v[98:101], v187, v187 op_sel_hi:[0,0,0]
	v_mfma_scale_f32_16x16x128_f8f6f4 v[86:89], v[10:17], v[196:203], v[86:89], v187, v187 op_sel_hi:[0,0,0]
	v_mfma_scale_f32_16x16x128_f8f6f4 v[82:85], v[2:9], v[196:203], v[82:85], v187, v187 op_sel_hi:[0,0,0]
	v_mfma_scale_f32_16x16x128_f8f6f4 v[78:81], v[10:17], v[204:211], v[78:81], v187, v187 op_sel_hi:[0,0,0]
	v_mfma_scale_f32_16x16x128_f8f6f4 v[74:77], v[2:9], v[204:211], v[74:77], v187, v187 op_sel_hi:[0,0,0]
	v_mfma_scale_f32_16x16x128_f8f6f4 v[70:73], v[10:17], v[212:219], v[70:73], v187, v187 op_sel_hi:[0,0,0]
	v_mfma_scale_f32_16x16x128_f8f6f4 v[66:69], v[2:9], v[212:219], v[66:69], v187, v187 op_sel_hi:[0,0,0]
	s_setprio 0
	s_barrier
	s_add_i32 s0, s62, s53
	v_lshl_add_u64 v[178:179], s[42:43], 0, v[164:165]
	s_mov_b32 m0, s0
	ds_read_b128 v[188:191], v186 offset:16384
	ds_read_b128 v[192:195], v186 offset:17408
	ds_read_b128 v[196:199], v186 offset:18432
	ds_read_b128 v[200:203], v186 offset:19456
	ds_read_b128 v[204:207], v186 offset:20480
	ds_read_b128 v[208:211], v186 offset:21504
	ds_read_b128 v[212:215], v186 offset:22528
	ds_read_b128 v[216:219], v186 offset:23552
	global_load_lds_dwordx4 v[178:179], off
	s_add_i32 m0, s0, 0x2000
	s_add_u32 s0, s42, 0x40000
	v_lshl_add_u64 v[178:179], s[42:43], 0, v[168:169]
	s_addc_u32 s1, s43, 0
	s_add_i32 s2, s63, s53
	global_load_lds_dwordx4 v[178:179], off
	v_lshl_add_u64 v[178:179], s[0:1], 0, v[164:165]
	s_mov_b32 m0, s2
	v_lshl_add_u64 v[180:181], s[44:45], 0, v[166:167]
	global_load_lds_dwordx4 v[178:179], off
	v_lshl_add_u64 v[178:179], s[0:1], 0, v[168:169]
	s_add_i32 m0, s2, 0x2000
	s_nop 0
	global_load_lds_dwordx4 v[178:179], off
	v_lshl_add_u64 v[178:179], s[44:45], 0, v[162:163]
	s_mov_b32 m0, s37
	s_nop 0
	global_load_lds_dwordx4 v[178:179], off
	s_mov_b32 m0, s54
	s_nop 0
	global_load_lds_dwordx4 v[180:181], off
	s_waitcnt vmcnt(8)
	s_waitcnt lgkmcnt(0)
	s_barrier
	s_setprio 1
	s_waitcnt lgkmcnt(0)
	v_mfma_scale_f32_16x16x128_f8f6f4 v[126:129], v[26:33], v[188:195], v[126:129], v187, v187 op_sel_hi:[0,0,0]
	v_mfma_scale_f32_16x16x128_f8f6f4 v[122:125], v[18:25], v[188:195], v[122:125], v187, v187 op_sel_hi:[0,0,0]
	v_mfma_scale_f32_16x16x128_f8f6f4 v[118:121], v[26:33], v[196:203], v[118:121], v187, v187 op_sel_hi:[0,0,0]
	v_mfma_scale_f32_16x16x128_f8f6f4 v[114:117], v[18:25], v[196:203], v[114:117], v187, v187 op_sel_hi:[0,0,0]
	v_mfma_scale_f32_16x16x128_f8f6f4 v[110:113], v[26:33], v[204:211], v[110:113], v187, v187 op_sel_hi:[0,0,0]
	v_mfma_scale_f32_16x16x128_f8f6f4 v[106:109], v[18:25], v[204:211], v[106:109], v187, v187 op_sel_hi:[0,0,0]
	v_mfma_scale_f32_16x16x128_f8f6f4 v[94:97], v[26:33], v[212:219], v[94:97], v187, v187 op_sel_hi:[0,0,0]
	v_mfma_scale_f32_16x16x128_f8f6f4 v[90:93], v[18:25], v[212:219], v[90:93], v187, v187 op_sel_hi:[0,0,0]
	v_mfma_scale_f32_16x16x128_f8f6f4 v[62:65], v[10:17], v[188:195], v[62:65], v187, v187 op_sel_hi:[0,0,0]
	v_mfma_scale_f32_16x16x128_f8f6f4 v[58:61], v[2:9], v[188:195], v[58:61], v187, v187 op_sel_hi:[0,0,0]
	v_mfma_scale_f32_16x16x128_f8f6f4 v[54:57], v[10:17], v[196:203], v[54:57], v187, v187 op_sel_hi:[0,0,0]
	v_mfma_scale_f32_16x16x128_f8f6f4 v[50:53], v[2:9], v[196:203], v[50:53], v187, v187 op_sel_hi:[0,0,0]
	v_mfma_scale_f32_16x16x128_f8f6f4 v[46:49], v[10:17], v[204:211], v[46:49], v187, v187 op_sel_hi:[0,0,0]
	v_mfma_scale_f32_16x16x128_f8f6f4 v[42:45], v[2:9], v[204:211], v[42:45], v187, v187 op_sel_hi:[0,0,0]
	v_mfma_scale_f32_16x16x128_f8f6f4 v[38:41], v[10:17], v[212:219], v[38:41], v187, v187 op_sel_hi:[0,0,0]
	v_mfma_scale_f32_16x16x128_f8f6f4 v[34:37], v[2:9], v[212:219], v[34:37], v187, v187 op_sel_hi:[0,0,0]
	s_setprio 0
	s_barrier
.Lmid_1577:
	s_add_i32 s2, 0, 0x18000
	v_add_u32_e32 v0, s2, v182
	s_add_i32 s3, 0, 0x1c000
	ds_read_b128 v[2:5], v0
	ds_read_b128 v[6:9], v0 offset:1024
	ds_read_b128 v[10:13], v0 offset:2048
	ds_read_b128 v[14:17], v0 offset:3072
	v_add_u32_e32 v0, s3, v182
	ds_read_b128 v[18:21], v0
	ds_read_b128 v[22:25], v0 offset:1024
	ds_read_b128 v[26:29], v0 offset:2048
	ds_read_b128 v[30:33], v0 offset:3072
	s_add_u32 s0, s44, 0x40000
	s_addc_u32 s1, s45, 0
	s_mov_b32 m0, s55
	v_lshl_add_u64 v[220:221], s[0:1], 0, v[162:163]
	ds_read_b128 v[188:191], v186 offset:32768
	ds_read_b128 v[192:195], v186 offset:33792
	ds_read_b128 v[196:199], v186 offset:34816
	ds_read_b128 v[200:203], v186 offset:35840
	ds_read_b128 v[204:207], v186 offset:36864
	ds_read_b128 v[208:211], v186 offset:37888
	ds_read_b128 v[212:215], v186 offset:38912
	ds_read_b128 v[216:219], v186 offset:39936
	global_load_lds_dwordx4 v[220:221], off
	v_lshl_add_u64 v[220:221], s[0:1], 0, v[166:167]
	s_mov_b32 m0, s56
	s_nop 0
	global_load_lds_dwordx4 v[220:221], off
	s_waitcnt vmcnt(8)
	s_waitcnt lgkmcnt(0)
	s_barrier
	s_setprio 1
	s_waitcnt lgkmcnt(0)
	v_mfma_scale_f32_16x16x128_f8f6f4 v[158:161], v[2:9], v[188:195], v[158:161], v187, v187 op_sel_hi:[0,0,0]
	v_mfma_scale_f32_16x16x128_f8f6f4 v[154:157], v[10:17], v[188:195], v[154:157], v187, v187 op_sel_hi:[0,0,0]
	v_mfma_scale_f32_16x16x128_f8f6f4 v[150:153], v[2:9], v[196:203], v[150:153], v187, v187 op_sel_hi:[0,0,0]
	v_mfma_scale_f32_16x16x128_f8f6f4 v[146:149], v[10:17], v[196:203], v[146:149], v187, v187 op_sel_hi:[0,0,0]
	v_mfma_scale_f32_16x16x128_f8f6f4 v[142:145], v[2:9], v[204:211], v[142:145], v187, v187 op_sel_hi:[0,0,0]
	v_mfma_scale_f32_16x16x128_f8f6f4 v[138:141], v[10:17], v[204:211], v[138:141], v187, v187 op_sel_hi:[0,0,0]
	v_mfma_scale_f32_16x16x128_f8f6f4 v[134:137], v[2:9], v[212:219], v[134:137], v187, v187 op_sel_hi:[0,0,0]
	v_mfma_scale_f32_16x16x128_f8f6f4 v[130:133], v[10:17], v[212:219], v[130:133], v187, v187 op_sel_hi:[0,0,0]
	v_mfma_scale_f32_16x16x128_f8f6f4 v[102:105], v[18:25], v[188:195], v[102:105], v187, v187 op_sel_hi:[0,0,0]
	v_mfma_scale_f32_16x16x128_f8f6f4 v[98:101], v[26:33], v[188:195], v[98:101], v187, v187 op_sel_hi:[0,0,0]
	v_mfma_scale_f32_16x16x128_f8f6f4 v[86:89], v[18:25], v[196:203], v[86:89], v187, v187 op_sel_hi:[0,0,0]
	v_mfma_scale_f32_16x16x128_f8f6f4 v[82:85], v[26:33], v[196:203], v[82:85], v187, v187 op_sel_hi:[0,0,0]
	v_mfma_scale_f32_16x16x128_f8f6f4 v[78:81], v[18:25], v[204:211], v[78:81], v187, v187 op_sel_hi:[0,0,0]
	v_mfma_scale_f32_16x16x128_f8f6f4 v[74:77], v[26:33], v[204:211], v[74:77], v187, v187 op_sel_hi:[0,0,0]
	v_mfma_scale_f32_16x16x128_f8f6f4 v[70:73], v[18:25], v[212:219], v[70:73], v187, v187 op_sel_hi:[0,0,0]
	v_mfma_scale_f32_16x16x128_f8f6f4 v[66:69], v[26:33], v[212:219], v[66:69], v187, v187 op_sel_hi:[0,0,0]
	s_setprio 0
	s_barrier
	s_add_u32 s0, s42, 0x2000
	s_addc_u32 s1, s43, 0
	s_add_i32 s2, s2, s53
	v_lshl_add_u64 v[220:221], s[0:1], 0, v[164:165]
	s_mov_b32 m0, s2
	ds_read_b128 v[188:191], v186 offset:49152
	ds_read_b128 v[192:195], v186 offset:50176
	ds_read_b128 v[196:199], v186 offset:51200
	ds_read_b128 v[200:203], v186 offset:52224
	ds_read_b128 v[204:207], v186 offset:53248
	ds_read_b128 v[208:211], v186 offset:54272
	ds_read_b128 v[212:215], v186 offset:55296
	ds_read_b128 v[216:219], v186 offset:56320
	global_load_lds_dwordx4 v[220:221], off
	s_add_i32 m0, s2, 0x2000
	v_lshl_add_u64 v[220:221], s[0:1], 0, v[168:169]
	s_add_u32 s0, s42, 0x42000
	s_addc_u32 s1, s43, 0
	s_add_i32 s2, s3, s53
	global_load_lds_dwordx4 v[220:221], off
	v_lshl_add_u64 v[220:221], s[0:1], 0, v[164:165]
	s_mov_b32 m0, s2
	v_lshl_add_u64 v[178:179], v[178:179], 0, s[14:15]
	global_load_lds_dwordx4 v[220:221], off
	v_lshl_add_u64 v[220:221], s[0:1], 0, v[168:169]
	s_add_i32 m0, s2, 0x2000
	s_nop 0
	global_load_lds_dwordx4 v[220:221], off
	s_mov_b32 m0, s58
	s_nop 0
	global_load_lds_dwordx4 v[178:179], off
	v_lshl_add_u64 v[178:179], v[180:181], 0, s[14:15]
	s_mov_b32 m0, s59
	s_nop 0
	global_load_lds_dwordx4 v[178:179], off
	s_waitcnt vmcnt(8)
	s_waitcnt lgkmcnt(0)
	s_barrier
	s_setprio 1
	s_waitcnt lgkmcnt(0)
	v_mfma_scale_f32_16x16x128_f8f6f4 v[126:129], v[2:9], v[188:195], v[126:129], v187, v187 op_sel_hi:[0,0,0]
	v_mfma_scale_f32_16x16x128_f8f6f4 v[122:125], v[10:17], v[188:195], v[122:125], v187, v187 op_sel_hi:[0,0,0]
	v_mfma_scale_f32_16x16x128_f8f6f4 v[118:121], v[2:9], v[196:203], v[118:121], v187, v187 op_sel_hi:[0,0,0]
	v_mfma_scale_f32_16x16x128_f8f6f4 v[114:117], v[10:17], v[196:203], v[114:117], v187, v187 op_sel_hi:[0,0,0]
	v_mfma_scale_f32_16x16x128_f8f6f4 v[110:113], v[2:9], v[204:211], v[110:113], v187, v187 op_sel_hi:[0,0,0]
	v_mfma_scale_f32_16x16x128_f8f6f4 v[106:109], v[10:17], v[204:211], v[106:109], v187, v187 op_sel_hi:[0,0,0]
	v_mfma_scale_f32_16x16x128_f8f6f4 v[94:97], v[2:9], v[212:219], v[94:97], v187, v187 op_sel_hi:[0,0,0]
	v_mfma_scale_f32_16x16x128_f8f6f4 v[90:93], v[10:17], v[212:219], v[90:93], v187, v187 op_sel_hi:[0,0,0]
	v_mfma_scale_f32_16x16x128_f8f6f4 v[62:65], v[18:25], v[188:195], v[62:65], v187, v187 op_sel_hi:[0,0,0]
	v_mfma_scale_f32_16x16x128_f8f6f4 v[58:61], v[26:33], v[188:195], v[58:61], v187, v187 op_sel_hi:[0,0,0]
	v_mfma_scale_f32_16x16x128_f8f6f4 v[54:57], v[18:25], v[196:203], v[54:57], v187, v187 op_sel_hi:[0,0,0]
	v_mfma_scale_f32_16x16x128_f8f6f4 v[50:53], v[26:33], v[196:203], v[50:53], v187, v187 op_sel_hi:[0,0,0]
	v_mfma_scale_f32_16x16x128_f8f6f4 v[46:49], v[18:25], v[204:211], v[46:49], v187, v187 op_sel_hi:[0,0,0]
	v_mfma_scale_f32_16x16x128_f8f6f4 v[42:45], v[26:33], v[204:211], v[42:45], v187, v187 op_sel_hi:[0,0,0]
	v_mfma_scale_f32_16x16x128_f8f6f4 v[38:41], v[18:25], v[212:219], v[38:41], v187, v187 op_sel_hi:[0,0,0]
	v_mfma_scale_f32_16x16x128_f8f6f4 v[34:37], v[26:33], v[212:219], v[34:37], v187, v187 op_sel_hi:[0,0,0]
	s_setprio 0
	s_barrier
	s_add_i32 s71, s71, 2
	s_add_u32 s69, s69, 0x4000
	s_addc_u32 s70, s70, 0
	s_add_u32 s40, s40, 0x100
	s_addc_u32 s41, s41, 0
	s_cmp_gt_u32 s71, 13
	s_cbranch_scc0 .LBB0_1577
	s_and_b64 vcc, exec, s[16:17]
	s_cbranch_vccz .LBB0_1580
	s_barrier
